# gMLP group loop software-pipelined: next group's weight tile, activation rows and LN bias (16 loads) issued behind the tile barrier, accumulators moved to the dead gain registers
# baseline (speedup 1.0000x reference)
; __device__ __forceinline__ void unpk8(const u32x4 w, f32x4& a, f32x4& b) { a = (f32x4){bflo(w.x), bfhi(w.x), bflo(w.y), bfhi(w.y)}; b = (f32x4){bflo(w.z), bfhi(w.z), bflo(w.w), bfhi(w.w)}; }
; #define LAS __attribute__((address_space(3)))
; __device__ __forceinline__ void gmlp_unit(Frame& F, const Args& a, int layer, int unit) {
;     ...
;     for (int g = 0; g < 8; ++g) {
; #pragma unroll
;         for (int i = 0; i < 4; ++i) { const int pc = tid + 512 * i, rr = pc >> 4, c16 = pc & 15;
;             *(LAS v4u*)(sA + rr * TP + c16 * 8) = *(const v4u*)(GMW + (size_t)g * 16384 + rr * 128 + c16 * 8); }
;         { const int p = tid & 127, oc0 = tid >> 7; const float mean = st[p * 2], rstd = st[p * 2 + 1];
; #pragma unroll
;           for (int i = 0; i < 4; ++i) { const int oc = oc0 + 4 * i, c0 = g * 128 + oc * 8;
;               f32x4 x0, x1; unpk8(*(const v4u*)(GUV + (t0 + p) * 2048 + 1024 + c0), x0, x1);
;               const f32x4 g0 = *(const f32x4*)(lng + c0), g1 = *(const f32x4*)(lng + c0 + 4), b0 = *(const f32x4*)(lnb + c0), b1 = *(const f32x4*)(lnb + c0 + 4);
.LBB0_832:
	s_lshl_b32 s22, s5, 1
	v_and_b32_e32 v19, 15, v6
	v_and_b32_e32 v4, -16, v6
	s_ashr_i32 s23, s22, 31
	v_add_u32_e32 v3, s27, v6
	v_add_u32_e32 v20, 0, v4
	v_or_b32_e32 v7, s75, v19
	v_or_b32_e32 v4, s77, v19
	v_ashrrev_i32_e32 v6, 2, v6
	s_lshl_b64 s[38:39], s[22:23], 7
	v_mul_u32_u24_e32 v22, 0x110, v7
	v_and_b32_e32 v23, -4, v6
	v_or_b32_e32 v6, 48, v4
	v_mov_b32_e32 v7, v0
	s_add_u32 s42, s6, 0x28400000
	v_lshl_add_u64 v[6:7], s[38:39], 0, v[6:7]
	s_addc_u32 s43, s7, 0
	v_ashrrev_i32_e32 v5, 4, v3
	s_movk_i32 s3, 0x110
	v_lshlrev_b64 v[6:7], 12, v[6:7]
	v_and_b32_e32 v1, 0x78, v2
	v_and_b32_e32 v2, -8, v5
	v_lshl_add_u64 v[26:27], s[42:43], 0, v[6:7]
	v_lshlrev_b32_e32 v6, 7, v5
	v_mul_lo_u32 v24, v5, s3
	v_add_u32_e32 v5, 0x200, v3
	v_ashrrev_i32_e32 v5, 4, v5
	v_lshlrev_b32_e32 v8, 7, v5
	v_mul_lo_u32 v25, v5, s3
	v_add_u32_e32 v5, 0x400, v3
	v_ashrrev_i32_e32 v5, 4, v5
	v_lshlrev_b32_e32 v10, 7, v5
	v_mul_lo_u32 v41, v5, s3
	v_mov_b32_e32 v5, v0
	v_lshl_add_u64 v[14:15], s[38:39], 0, v[4:5]
	v_lshlrev_b64 v[14:15], 12, v[14:15]
	v_mul_lo_u32 v21, v4, s3
	v_lshl_add_u64 v[28:29], s[42:43], 0, v[14:15]
	v_or_b32_e32 v14, 16, v4
	v_or_b32_e32 v4, 32, v4
	v_mov_b32_e32 v15, v0
	v_lshl_add_u64 v[4:5], s[38:39], 0, v[4:5]
	v_lshl_add_u64 v[14:15], s[38:39], 0, v[14:15]
	v_lshlrev_b64 v[4:5], 12, v[4:5]
	v_lshlrev_b64 v[14:15], 12, v[14:15]
	v_lshl_add_u64 v[32:33], s[42:43], 0, v[4:5]
	v_lshlrev_b32_e32 v4, 4, v19
	v_mov_b32_e32 v5, v0
	v_ashrrev_i32_e32 v7, 31, v6
	v_lshl_add_u64 v[30:31], s[42:43], 0, v[14:15]
	v_lshl_add_u64 v[4:5], s[0:1], 0, v[4:5]
	v_readlane_b32 s40, v251, 34
	v_and_b32_e32 v17, 0x7f, v3
	v_add_u32_e32 v3, 0x600, v3
	v_lshl_add_u64 v[34:35], v[6:7], 1, v[4:5]
	v_add_u32_e32 v6, s77, v19
	v_mov_b32_e32 v7, v0
	v_readlane_b32 s52, v251, 46
	v_readlane_b32 s53, v251, 47
	s_add_u32 s36, s36, 0x28400880
	v_ashrrev_i32_e32 v3, 4, v3
	v_lshl_add_u64 v[38:39], v[6:7], 2, s[52:53]
	s_addc_u32 s37, s37, 0
	v_lshlrev_b32_e32 v6, 12, v17
	v_lshl_add_u32 v16, v1, 1, 0
	v_lshl_add_u32 v1, v17, 3, 0
	v_lshlrev_b32_e32 v12, 7, v3
	v_mul_lo_u32 v52, v3, s3
	v_lshl_add_u64 v[6:7], s[36:37], 0, v[6:7]
	v_ashrrev_i32_e32 v3, 31, v2
	v_mad_i32_i24 v18, v17, -6, v1
	v_ashrrev_i32_e32 v9, 31, v8
	v_ashrrev_i32_e32 v11, 31, v10
	v_ashrrev_i32_e32 v13, 31, v12
	v_mul_lo_u32 v53, v2, s3
	v_readlane_b32 s46, v251, 40
	v_readlane_b32 s47, v251, 41
	v_readlane_b32 s48, v251, 42
	v_readlane_b32 s49, v251, 43
	v_lshl_add_u64 v[44:45], v[2:3], 1, v[6:7]
	v_lshlrev_b64 v[2:3], 2, v[2:3]
	v_lshl_add_u64 v[36:37], v[8:9], 1, v[4:5]
	v_add_u32_e32 v40, s75, v23
	v_lshl_add_u64 v[42:43], v[10:11], 1, v[4:5]
	v_lshl_add_u64 v[46:47], v[12:13], 1, v[4:5]
	v_lshl_add_u64 v[48:49], s[48:49], 0, v[2:3]
	v_lshl_add_u64 v[50:51], s[46:47], 0, v[2:3]
	s_mov_b64 s[36:37], 0
	v_add_u32_e32 v56, v16, v24
	v_add_u32_e32 v57, v16, v25
	v_add_u32_e32 v58, v16, v41
	v_add_u32_e32 v59, v16, v52
	v_add_u32_e32 v60, v18, v53
	v_add_u32_e32 v61, v20, v21
	v_add_u32_e32 v62, v20, v22
	s_waitcnt lgkmcnt(0)
	s_barrier
	v_readlane_b32 s41, v251, 35
	v_readlane_b32 s42, v251, 36
	v_readlane_b32 s43, v251, 37
	v_readlane_b32 s44, v251, 38
	v_readlane_b32 s45, v251, 39
	v_readlane_b32 s50, v251, 44
	v_readlane_b32 s51, v251, 45
	v_readlane_b32 s54, v251, 48
	v_readlane_b32 s55, v251, 49
	v_lshl_add_u64 v[2:3], s[6:7], 0, v[34:35]
	global_load_dwordx4 v[100:103], v[2:3], off
	v_lshl_add_u64 v[34:35], v[34:35], 0, s[34:35]
	v_lshl_add_u64 v[2:3], s[6:7], 0, v[36:37]
	global_load_dwordx4 v[104:107], v[2:3], off
	v_lshl_add_u64 v[36:37], v[36:37], 0, s[34:35]
	v_lshl_add_u64 v[2:3], s[6:7], 0, v[42:43]
	global_load_dwordx4 v[108:111], v[2:3], off
	v_lshl_add_u64 v[42:43], v[42:43], 0, s[34:35]
	v_lshl_add_u64 v[2:3], s[6:7], 0, v[46:47]
	global_load_dwordx4 v[112:115], v[2:3], off
	v_lshl_add_u64 v[46:47], v[46:47], 0, s[34:35]
	v_lshl_add_u64 v[4:5], s[6:7], 0, v[44:45]
	v_lshl_add_u64 v[6:7], v[48:49], 0, s[36:37]
	v_lshl_add_u64 v[44:45], v[44:45], 0, s[66:67]
	global_load_dwordx4 v[116:119], v[4:5], off offset:-128
	global_load_dwordx4 v[120:123], v[4:5], off offset:-64
	global_load_dwordx4 v[124:127], v[4:5], off
	global_load_dwordx4 v[128:131], v[4:5], off offset:64
	global_load_dwordx4 v[164:167], v[6:7], off
	global_load_dwordx4 v[168:171], v[6:7], off offset:16
	global_load_dwordx4 v[172:175], v[6:7], off offset:128
	global_load_dwordx4 v[176:179], v[6:7], off offset:144
	global_load_dwordx4 v[180:183], v[6:7], off offset:256
	global_load_dwordx4 v[184:187], v[6:7], off offset:272
	global_load_dwordx4 v[188:191], v[6:7], off offset:384
	global_load_dwordx4 v[192:195], v[6:7], off offset:400
; __device__ __forceinline__ void unpk8(const u32x4 w, f32x4& a, f32x4& b) { a = (f32x4){bflo(w.x), bfhi(w.x), bflo(w.y), bfhi(w.y)}; b = (f32x4){bflo(w.z), bfhi(w.z), bflo(w.w), bfhi(w.w)}; }
; __device__ __forceinline__ u32x4 pk8(const f32x4 a, const f32x4 b) { u32x4 w; w.x = cvt_pk_bf16(a[0], a[1]); w.y = cvt_pk_bf16(a[2], a[3]); w.z = cvt_pk_bf16(b[0], b[1]); w.w = cvt_pk_bf16(b[2], b[3]); return w; }
; #define LAS __attribute__((address_space(3)))
; __device__ __forceinline__ void gmlp_unit(Frame& F, const Args& a, int layer, int unit) {
;     ...
;         for (int i = 0; i < 4; ++i) { const int pc = tid + 512 * i, rr = pc >> 4, c16 = pc & 15;
;             *(LAS v4u*)(sA + rr * TP + c16 * 8) = *(const v4u*)(GMW + (size_t)g * 16384 + rr * 128 + c16 * 8); }
;         { const int p = tid & 127, oc0 = tid >> 7; const float mean = st[p * 2], rstd = st[p * 2 + 1];
; #pragma unroll
;           for (int i = 0; i < 4; ++i) { const int oc = oc0 + 4 * i, c0 = g * 128 + oc * 8;
;               f32x4 x0, x1; unpk8(*(const v4u*)(GUV + (t0 + p) * 2048 + 1024 + c0), x0, x1);
;               const f32x4 g0 = *(const f32x4*)(lng + c0), g1 = *(const f32x4*)(lng + c0 + 4), b0 = *(const f32x4*)(lnb + c0), b1 = *(const f32x4*)(lnb + c0 + 4);
;               x0 = (x0 - mean) * rstd * g0 + b0; x1 = (x1 - mean) * rstd * g1 + b1;
;               const v4u w = pk8(x0, x1);
;               LAS bf16* d = sB + (oc * 8) * TP + p;
;               d[0 * TP] = (bf16)(w.x & 0xffffu); d[1 * TP] = (bf16)(w.x >> 16); d[2 * TP] = (bf16)(w.y & 0xffffu); d[3 * TP] = (bf16)(w.y >> 16);
;               d[4 * TP] = (bf16)(w.z & 0xffffu); d[5 * TP] = (bf16)(w.z >> 16); d[6 * TP] = (bf16)(w.w & 0xffffu); d[7 * TP] = (bf16)(w.w >> 16); } }
.LBB0_833:
	ds_read_b64 v[2:3], v1
	v_ashrrev_i32_e32 v41, 31, v40
	v_lshl_add_u64 v[54:55], v[38:39], 0, s[36:37]
	v_lshlrev_b64 v[52:53], 1, v[40:41]
	v_add_u32_e32 v40, 0x80, v40
	v_lshl_add_u64 v[232:233], v[28:29], 0, v[52:53]
	v_lshl_add_u64 v[234:235], v[30:31], 0, v[52:53]
	v_lshl_add_u64 v[236:237], v[32:33], 0, v[52:53]
	v_lshl_add_u64 v[238:239], v[26:27], 0, v[52:53]
	v_lshl_add_u64 v[8:9], v[50:51], 0, s[36:37]
	global_load_dwordx4 v[132:135], v[8:9], off
	global_load_dwordx4 v[136:139], v[8:9], off offset:16
	global_load_dwordx4 v[140:143], v[8:9], off offset:128
	global_load_dwordx4 v[144:147], v[8:9], off offset:144
	global_load_dwordx4 v[148:151], v[8:9], off offset:256
	global_load_dwordx4 v[152:155], v[8:9], off offset:272
	global_load_dwordx4 v[156:159], v[8:9], off offset:384
	global_load_dwordx4 v[160:163], v[8:9], off offset:400
	global_load_dword v196, v[54:55], off
	global_load_dwordx2 v[204:205], v[232:233], off
	global_load_dwordx2 v[206:207], v[232:233], off offset:32
	global_load_dword v198, v[54:55], off offset:64
	global_load_dwordx2 v[224:225], v[234:235], off
	global_load_dwordx2 v[226:227], v[234:235], off offset:32
	global_load_dword v200, v[54:55], off offset:128
	global_load_dwordx2 v[228:229], v[236:237], off
	global_load_dwordx2 v[230:231], v[236:237], off offset:32
	global_load_dword v202, v[54:55], off offset:192
	global_load_dwordx2 v[246:247], v[238:239], off
	global_load_dwordx2 v[248:249], v[238:239], off offset:32
	s_waitcnt vmcnt(35)
	ds_write_b128 v56, v[100:103] offset:1024
	s_waitcnt vmcnt(34)
	ds_write_b128 v57, v[104:107] offset:1024
	s_waitcnt vmcnt(33)
	ds_write_b128 v58, v[108:111] offset:1024
	s_waitcnt vmcnt(32)
	ds_write_b128 v59, v[112:115] offset:1024
	s_waitcnt lgkmcnt(4)
	s_waitcnt vmcnt(18)
	v_lshlrev_b32_e32 v41, 16, v116
	v_and_b32_e32 v54, 0xffff0000, v116
	v_lshlrev_b32_e32 v52, 16, v117
	v_and_b32_e32 v53, 0xffff0000, v117
	v_lshlrev_b32_e32 v63, 16, v118
	v_and_b32_e32 v64, 0xffff0000, v118
	v_lshlrev_b32_e32 v65, 16, v119
	v_and_b32_e32 v66, 0xffff0000, v119
	v_sub_f32_e32 v53, v53, v2
	v_sub_f32_e32 v52, v52, v2
	v_sub_f32_e32 v55, v54, v2
	v_sub_f32_e32 v54, v41, v2
	v_pk_mul_f32 v[52:53], v[2:3], v[52:53] op_sel:[1,0]
	v_pk_mul_f32 v[54:55], v[2:3], v[54:55] op_sel:[1,0]
	v_pk_fma_f32 v[134:135], v[134:135], v[52:53], v[166:167]
	v_sub_f32_e32 v167, v64, v2
	v_sub_f32_e32 v166, v63, v2
	v_pk_fma_f32 v[132:133], v[132:133], v[54:55], v[164:165]
	v_sub_f32_e32 v165, v66, v2
	v_sub_f32_e32 v164, v65, v2
	v_pk_mul_f32 v[166:167], v[2:3], v[166:167] op_sel:[1,0]
	v_pk_mul_f32 v[164:165], v[2:3], v[164:165] op_sel:[1,0]
	v_pk_fma_f32 v[136:137], v[136:137], v[166:167], v[168:169]
	v_cvt_pk_bf16_f32 v132, v132, v133
	v_pk_fma_f32 v[138:139], v[138:139], v[164:165], v[170:171]
	v_cvt_pk_bf16_f32 v133, v134, v135
	v_cvt_pk_bf16_f32 v136, v136, v137
	s_nop 0
	v_cvt_pk_bf16_f32 v137, v138, v139
	ds_write_b16 v60, v132 offset:35840
	ds_write_b16_d16_hi v60, v132 offset:36112
	ds_write_b16 v60, v133 offset:36384
	ds_write_b16_d16_hi v60, v133 offset:36656
	ds_write_b16 v60, v136 offset:36928
	ds_write_b16_d16_hi v60, v136 offset:37200
	ds_write_b16 v60, v137 offset:37472
	ds_write_b16_d16_hi v60, v137 offset:37744
	s_waitcnt vmcnt(16)
	v_lshlrev_b32_e32 v41, 16, v120
	v_and_b32_e32 v54, 0xffff0000, v120
	v_lshlrev_b32_e32 v52, 16, v121
	v_and_b32_e32 v53, 0xffff0000, v121
	v_lshlrev_b32_e32 v63, 16, v122
	v_and_b32_e32 v64, 0xffff0000, v122
	v_lshlrev_b32_e32 v65, 16, v123
	v_and_b32_e32 v66, 0xffff0000, v123
	v_sub_f32_e32 v53, v53, v2
	v_sub_f32_e32 v52, v52, v2
	v_sub_f32_e32 v55, v54, v2
	v_sub_f32_e32 v54, v41, v2
	v_pk_mul_f32 v[52:53], v[2:3], v[52:53] op_sel:[1,0]
	v_pk_mul_f32 v[54:55], v[2:3], v[54:55] op_sel:[1,0]
	v_pk_fma_f32 v[142:143], v[142:143], v[52:53], v[174:175]
	v_sub_f32_e32 v175, v64, v2
	v_sub_f32_e32 v174, v63, v2
	v_pk_fma_f32 v[140:141], v[140:141], v[54:55], v[172:173]
	v_sub_f32_e32 v173, v66, v2
	v_sub_f32_e32 v172, v65, v2
	v_pk_mul_f32 v[174:175], v[2:3], v[174:175] op_sel:[1,0]
	v_pk_mul_f32 v[172:173], v[2:3], v[172:173] op_sel:[1,0]
	v_pk_fma_f32 v[144:145], v[144:145], v[174:175], v[176:177]
	v_cvt_pk_bf16_f32 v140, v140, v141
	v_pk_fma_f32 v[146:147], v[146:147], v[172:173], v[178:179]
	v_cvt_pk_bf16_f32 v141, v142, v143
	v_cvt_pk_bf16_f32 v144, v144, v145
	s_nop 0
	v_cvt_pk_bf16_f32 v145, v146, v147
	ds_write_b16 v60, v140 offset:44544
	ds_write_b16_d16_hi v60, v140 offset:44816
	ds_write_b16 v60, v141 offset:45088
	ds_write_b16_d16_hi v60, v141 offset:45360
	ds_write_b16 v60, v144 offset:45632
	ds_write_b16_d16_hi v60, v144 offset:45904
	ds_write_b16 v60, v145 offset:46176
	ds_write_b16_d16_hi v60, v145 offset:46448
	s_waitcnt vmcnt(14)
	v_lshlrev_b32_e32 v41, 16, v124
	v_and_b32_e32 v54, 0xffff0000, v124
	v_lshlrev_b32_e32 v52, 16, v125
	v_and_b32_e32 v53, 0xffff0000, v125
	v_lshlrev_b32_e32 v63, 16, v126
	v_and_b32_e32 v64, 0xffff0000, v126
	v_lshlrev_b32_e32 v65, 16, v127
	v_and_b32_e32 v66, 0xffff0000, v127
	v_sub_f32_e32 v53, v53, v2
	v_sub_f32_e32 v52, v52, v2
	v_sub_f32_e32 v55, v54, v2
	v_sub_f32_e32 v54, v41, v2
	v_pk_mul_f32 v[52:53], v[2:3], v[52:53] op_sel:[1,0]
	v_pk_mul_f32 v[54:55], v[2:3], v[54:55] op_sel:[1,0]
	v_pk_fma_f32 v[150:151], v[150:151], v[52:53], v[182:183]
	v_sub_f32_e32 v183, v64, v2
	v_sub_f32_e32 v182, v63, v2
	v_pk_fma_f32 v[148:149], v[148:149], v[54:55], v[180:181]
	v_sub_f32_e32 v181, v66, v2
	v_sub_f32_e32 v180, v65, v2
	v_pk_mul_f32 v[182:183], v[2:3], v[182:183] op_sel:[1,0]
	v_pk_mul_f32 v[180:181], v[2:3], v[180:181] op_sel:[1,0]
	v_pk_fma_f32 v[152:153], v[152:153], v[182:183], v[184:185]
	v_cvt_pk_bf16_f32 v148, v148, v149
	v_pk_fma_f32 v[154:155], v[154:155], v[180:181], v[186:187]
	v_cvt_pk_bf16_f32 v149, v150, v151
	v_cvt_pk_bf16_f32 v152, v152, v153
	s_nop 0
	v_cvt_pk_bf16_f32 v153, v154, v155
	ds_write_b16 v60, v148 offset:53248
	ds_write_b16_d16_hi v60, v148 offset:53520
	ds_write_b16 v60, v149 offset:53792
	ds_write_b16_d16_hi v60, v149 offset:54064
	ds_write_b16 v60, v152 offset:54336
	ds_write_b16_d16_hi v60, v152 offset:54608
	ds_write_b16 v60, v153 offset:54880
	ds_write_b16_d16_hi v60, v153 offset:55152
	s_waitcnt vmcnt(12)
; __device__ __forceinline__ void unpk8(const u32x4 w, f32x4& a, f32x4& b) { a = (f32x4){bflo(w.x), bfhi(w.x), bflo(w.y), bfhi(w.y)}; b = (f32x4){bflo(w.z), bfhi(w.z), bflo(w.w), bfhi(w.w)}; }
; #define LAS __attribute__((address_space(3)))
; __device__ __forceinline__ void mma_128(const LAS bf16* sA, const LAS bf16* sBt, int wave, int lane, f32x4 (&acc)[4][2]) {
;     ...
;     for (int kk = 0; kk < 4; ++kk) {
;         bf16x8 af[4], bf_[2];
; #pragma unroll
;         for (int mt = 0; mt < 4; ++mt) af[mt] = *(const LAS bf16x8*)(sA + (64 * wm + 16 * mt + fr) * TP + 32 * kk + 8 * fq);
; #pragma unroll
;         for (int nt = 0; nt < 2; ++nt) bf_[nt] = *(const LAS bf16x8*)(sBt + (32 * wn + 16 * nt + fr) * TP + 32 * kk + 8 * fq);
; #pragma unroll
;         for (int mt = 0; mt < 4; ++mt)
; #pragma unroll
;             for (int nt = 0; nt < 2; ++nt) acc[mt][nt] = __builtin_amdgcn_mfma_f32_16x16x32_bf16(bf_[nt], af[mt], acc[mt][nt], 0, 0, 0);
; __device__ __forceinline__ void gmlp_unit(Frame& F, const Args& a, int layer, int unit) {
;     ...
;         { const int p = tid & 127, oc0 = tid >> 7; const float mean = st[p * 2], rstd = st[p * 2 + 1];
; #pragma unroll
;           for (int i = 0; i < 4; ++i) { const int oc = oc0 + 4 * i, c0 = g * 128 + oc * 8;
;               f32x4 x0, x1; unpk8(*(const v4u*)(GUV + (t0 + p) * 2048 + 1024 + c0), x0, x1);
;               const f32x4 g0 = *(const f32x4*)(lng + c0), g1 = *(const f32x4*)(lng + c0 + 4), b0 = *(const f32x4*)(lnb + c0), b1 = *(const f32x4*)(lnb + c0 + 4);
;               x0 = (x0 - mean) * rstd * g0 + b0; x1 = (x1 - mean) * rstd * g1 + b1;
;               const v4u w = pk8(x0, x1);
;               LAS bf16* d = sB + (oc * 8) * TP + p;
;               d[0 * TP] = (bf16)(w.x & 0xffffu); d[1 * TP] = (bf16)(w.x >> 16); d[2 * TP] = (bf16)(w.y & 0xffffu); d[3 * TP] = (bf16)(w.y >> 16);
;               d[4 * TP] = (bf16)(w.z & 0xffffu); d[5 * TP] = (bf16)(w.z >> 16); d[6 * TP] = (bf16)(w.w & 0xffffu); d[7 * TP] = (bf16)(w.w >> 16); } }
;         __syncthreads();
;         f32x4 acc[4][2];
; #pragma unroll
;         for (int mt = 0; mt < 4; ++mt)
; #pragma unroll
;             for (int nt = 0; nt < 2; ++nt) acc[mt][nt] = (f32x4){0.f, 0.f, 0.f, 0.f};
;         mma_128(sA, sB, wave, lane, acc);
	v_lshlrev_b32_e32 v41, 16, v128
	v_and_b32_e32 v54, 0xffff0000, v128
	v_lshlrev_b32_e32 v52, 16, v129
	v_and_b32_e32 v53, 0xffff0000, v129
	v_lshlrev_b32_e32 v63, 16, v130
	v_and_b32_e32 v64, 0xffff0000, v130
	v_lshlrev_b32_e32 v65, 16, v131
	v_and_b32_e32 v66, 0xffff0000, v131
	v_sub_f32_e32 v53, v53, v2
	v_sub_f32_e32 v52, v52, v2
	v_sub_f32_e32 v55, v54, v2
	v_sub_f32_e32 v54, v41, v2
	v_pk_mul_f32 v[52:53], v[2:3], v[52:53] op_sel:[1,0]
	v_pk_mul_f32 v[54:55], v[2:3], v[54:55] op_sel:[1,0]
	v_pk_fma_f32 v[158:159], v[158:159], v[52:53], v[190:191]
	v_sub_f32_e32 v191, v64, v2
	v_sub_f32_e32 v190, v63, v2
	v_pk_fma_f32 v[156:157], v[156:157], v[54:55], v[188:189]
	v_sub_f32_e32 v189, v66, v2
	v_sub_f32_e32 v188, v65, v2
	v_pk_mul_f32 v[190:191], v[2:3], v[190:191] op_sel:[1,0]
	v_pk_mul_f32 v[188:189], v[2:3], v[188:189] op_sel:[1,0]
	v_pk_fma_f32 v[160:161], v[160:161], v[190:191], v[192:193]
	v_cvt_pk_bf16_f32 v156, v156, v157
	v_pk_fma_f32 v[162:163], v[162:163], v[188:189], v[194:195]
	v_cvt_pk_bf16_f32 v157, v158, v159
	v_cvt_pk_bf16_f32 v160, v160, v161
	s_nop 0
	v_cvt_pk_bf16_f32 v161, v162, v163
	ds_write_b16 v60, v156 offset:61952
	ds_write_b16_d16_hi v60, v156 offset:62224
	ds_write_b16 v60, v157 offset:62496
	ds_write_b16_d16_hi v60, v157 offset:62768
	ds_write_b16 v60, v160 offset:63040
	ds_write_b16_d16_hi v60, v160 offset:63312
	ds_write_b16 v60, v161 offset:63584
	ds_write_b16_d16_hi v60, v161 offset:63856
	s_waitcnt lgkmcnt(0)
	s_barrier
	s_add_u32 s36, s36, 0x200
	s_addc_u32 s37, s37, 0
	s_cmpk_eq_i32 s36, 0x1000
	s_cbranch_scc1 .Lgm_u1_last
	v_lshl_add_u64 v[72:73], s[6:7], 0, v[34:35]
	global_load_dwordx4 v[100:103], v[72:73], off
	v_lshl_add_u64 v[34:35], v[34:35], 0, s[34:35]
	v_lshl_add_u64 v[72:73], s[6:7], 0, v[36:37]
	global_load_dwordx4 v[104:107], v[72:73], off
	v_lshl_add_u64 v[36:37], v[36:37], 0, s[34:35]
	v_lshl_add_u64 v[72:73], s[6:7], 0, v[42:43]
	global_load_dwordx4 v[108:111], v[72:73], off
	v_lshl_add_u64 v[42:43], v[42:43], 0, s[34:35]
	v_lshl_add_u64 v[72:73], s[6:7], 0, v[46:47]
	global_load_dwordx4 v[112:115], v[72:73], off
	v_lshl_add_u64 v[46:47], v[46:47], 0, s[34:35]
	v_lshl_add_u64 v[74:75], s[6:7], 0, v[44:45]
	v_lshl_add_u64 v[70:71], v[48:49], 0, s[36:37]
	v_lshl_add_u64 v[44:45], v[44:45], 0, s[66:67]
	global_load_dwordx4 v[116:119], v[74:75], off offset:-128
	global_load_dwordx4 v[120:123], v[74:75], off offset:-64
	global_load_dwordx4 v[124:127], v[74:75], off
	global_load_dwordx4 v[128:131], v[74:75], off offset:64
	global_load_dwordx4 v[164:167], v[70:71], off
	global_load_dwordx4 v[168:171], v[70:71], off offset:16
	global_load_dwordx4 v[172:175], v[70:71], off offset:128
	global_load_dwordx4 v[176:179], v[70:71], off offset:144
	global_load_dwordx4 v[180:183], v[70:71], off offset:256
	global_load_dwordx4 v[184:187], v[70:71], off offset:272
	global_load_dwordx4 v[188:191], v[70:71], off offset:384
	global_load_dwordx4 v[192:195], v[70:71], off offset:400
	ds_read_b128 v[2:5], v61 offset:1024
	ds_read_b128 v[6:9], v61 offset:5376
	ds_read_b128 v[10:13], v61 offset:9728
	ds_read_b128 v[14:17], v61 offset:14080
	ds_read_b128 v[18:21], v62 offset:35840
	ds_read_b128 v[22:25], v62 offset:40192
	ds_read_b128 v[84:87], v61 offset:1088
	ds_read_b128 v[88:91], v61 offset:5440
	ds_read_b128 v[92:95], v61 offset:9792
	ds_read_b128 v[96:99], v61 offset:14144
	ds_read_b128 v[76:79], v62 offset:35904
	ds_read_b128 v[80:83], v62 offset:40256
	s_waitcnt lgkmcnt(6)
	v_mfma_f32_16x16x32_bf16 v[132:135], v[18:21], v[2:5], 0
	v_mfma_f32_16x16x32_bf16 v[136:139], v[22:25], v[2:5], 0
	v_mfma_f32_16x16x32_bf16 v[140:143], v[18:21], v[6:9], 0
	v_mfma_f32_16x16x32_bf16 v[144:147], v[22:25], v[6:9], 0
	v_mfma_f32_16x16x32_bf16 v[148:151], v[18:21], v[10:13], 0
	v_mfma_f32_16x16x32_bf16 v[152:155], v[22:25], v[10:13], 0
	v_mfma_f32_16x16x32_bf16 v[156:159], v[18:21], v[14:17], 0
	v_mfma_f32_16x16x32_bf16 v[160:163], v[22:25], v[14:17], 0
	ds_read_b128 v[2:5], v61 offset:1152
	ds_read_b128 v[6:9], v61 offset:5504
	ds_read_b128 v[10:13], v61 offset:9856
	ds_read_b128 v[14:17], v61 offset:14208
	ds_read_b128 v[18:21], v62 offset:35968
	ds_read_b128 v[22:25], v62 offset:40320
	s_waitcnt lgkmcnt(6)
	v_mfma_f32_16x16x32_bf16 v[132:135], v[76:79], v[84:87], v[132:135]
	v_mfma_f32_16x16x32_bf16 v[136:139], v[80:83], v[84:87], v[136:139]
	v_mfma_f32_16x16x32_bf16 v[140:143], v[76:79], v[88:91], v[140:143]
	v_mfma_f32_16x16x32_bf16 v[144:147], v[80:83], v[88:91], v[144:147]
	v_mfma_f32_16x16x32_bf16 v[148:151], v[76:79], v[92:95], v[148:151]
	v_mfma_f32_16x16x32_bf16 v[152:155], v[80:83], v[92:95], v[152:155]
	v_mfma_f32_16x16x32_bf16 v[156:159], v[76:79], v[96:99], v[156:159]
	v_mfma_f32_16x16x32_bf16 v[160:163], v[80:83], v[96:99], v[160:163]
	ds_read_b128 v[84:87], v61 offset:1216
	ds_read_b128 v[88:91], v61 offset:5568
	ds_read_b128 v[92:95], v61 offset:9920
	ds_read_b128 v[96:99], v61 offset:14272
	ds_read_b128 v[76:79], v62 offset:36032
	ds_read_b128 v[80:83], v62 offset:40384
	s_waitcnt lgkmcnt(6)
	v_mfma_f32_16x16x32_bf16 v[132:135], v[18:21], v[2:5], v[132:135]
	v_mfma_f32_16x16x32_bf16 v[136:139], v[22:25], v[2:5], v[136:139]
	v_mfma_f32_16x16x32_bf16 v[140:143], v[18:21], v[6:9], v[140:143]
	v_mfma_f32_16x16x32_bf16 v[144:147], v[22:25], v[6:9], v[144:147]
	v_mfma_f32_16x16x32_bf16 v[148:151], v[18:21], v[10:13], v[148:151]
	v_mfma_f32_16x16x32_bf16 v[152:155], v[22:25], v[10:13], v[152:155]
	v_mfma_f32_16x16x32_bf16 v[156:159], v[18:21], v[14:17], v[156:159]
	v_mfma_f32_16x16x32_bf16 v[160:163], v[22:25], v[14:17], v[160:163]
	s_waitcnt lgkmcnt(0)
; __device__ __forceinline__ unsigned cvt_pk_bf16(float lo, float hi) { unsigned r; asm volatile("v_cvt_pk_bf16_f32 %0, %1, %2" : "=v"(r) : "v"(lo), "v"(hi)); return r; }
; __device__ __forceinline__ void gmlp_unit(Frame& F, const Args& a, int layer, int unit) {
;     ...
;         { const int wm = wave >> 2, wn = wave & 3, fr = lane & 15, fq = lane >> 4;
; #pragma unroll
;           for (int mt = 0; mt < 4; ++mt) { const int tt = 64 * wm + 16 * mt + fr; const float bsv = bsp[g * 128 + tt];
; #pragma unroll
;               for (int nt = 0; nt < 2; ++nt) { const int c = g * 128 + 32 * wn + 16 * nt + 4 * fq;
;                   const v2u uw = *(const v2u*)(GUV + (t0 + tt) * 2048 + c);
;                   const f32x4 u4 = (f32x4){bflo(uw.x), bfhi(uw.x), bflo(uw.y), bfhi(uw.y)};
;                   const f32x4 yb = u4 * (acc[mt][nt] + bsv);
;                   v2u ow; ow.x = cvt_pk_bf16(yb.x, yb.y); ow.y = cvt_pk_bf16(yb.z, yb.w);
;                   *(v2u*)(GUV + (t0 + tt) * 2048 + c) = ow; } } }
;         __syncthreads();
	v_mfma_f32_16x16x32_bf16 v[132:135], v[76:79], v[84:87], v[132:135]
	v_mfma_f32_16x16x32_bf16 v[136:139], v[80:83], v[84:87], v[136:139]
	v_mfma_f32_16x16x32_bf16 v[140:143], v[76:79], v[88:91], v[140:143]
	v_mfma_f32_16x16x32_bf16 v[144:147], v[80:83], v[88:91], v[144:147]
	v_mfma_f32_16x16x32_bf16 v[148:151], v[76:79], v[92:95], v[148:151]
	v_mfma_f32_16x16x32_bf16 v[152:155], v[80:83], v[92:95], v[152:155]
	v_mfma_f32_16x16x32_bf16 v[156:159], v[76:79], v[96:99], v[156:159]
	v_mfma_f32_16x16x32_bf16 v[160:163], v[80:83], v[96:99], v[160:163]
	s_nop 7
	s_nop 1
	s_waitcnt vmcnt(25)
	v_lshlrev_b32_e32 v70, 16, v204
	v_and_b32_e32 v71, 0xffff0000, v204
	v_lshlrev_b32_e32 v68, 16, v205
	v_and_b32_e32 v69, 0xffff0000, v205
	v_pk_add_f32 v[72:73], v[134:135], v[196:197] op_sel_hi:[1,0]
	v_pk_add_f32 v[74:75], v[132:133], v[196:197] op_sel_hi:[1,0]
	v_pk_mul_f32 v[68:69], v[72:73], v[68:69]
	v_pk_mul_f32 v[70:71], v[74:75], v[70:71]
	v_cvt_pk_bf16_f32 v70, v70, v71
	v_cvt_pk_bf16_f32 v71, v68, v69
	global_store_dwordx2 v[232:233], v[70:71], off
	v_lshlrev_b32_e32 v16, 16, v206
	v_and_b32_e32 v17, 0xffff0000, v206
	v_lshlrev_b32_e32 v18, 16, v207
	v_and_b32_e32 v19, 0xffff0000, v207
	v_pk_add_f32 v[20:21], v[136:137], v[196:197] op_sel_hi:[1,0]
	v_pk_add_f32 v[22:23], v[138:139], v[196:197] op_sel_hi:[1,0]
	v_pk_mul_f32 v[20:21], v[20:21], v[16:17]
	v_pk_mul_f32 v[22:23], v[22:23], v[18:19]
	v_cvt_pk_bf16_f32 v20, v20, v21
	s_nop 0
	v_cvt_pk_bf16_f32 v21, v22, v23
	global_store_dwordx2 v[232:233], v[20:21], off offset:32
	s_waitcnt vmcnt(24)
	v_lshlrev_b32_e32 v70, 16, v224
	v_and_b32_e32 v71, 0xffff0000, v224
	v_lshlrev_b32_e32 v68, 16, v225
	v_and_b32_e32 v69, 0xffff0000, v225
	v_pk_add_f32 v[72:73], v[142:143], v[198:199] op_sel_hi:[1,0]
	v_pk_add_f32 v[74:75], v[140:141], v[198:199] op_sel_hi:[1,0]
	v_pk_mul_f32 v[68:69], v[72:73], v[68:69]
	v_pk_mul_f32 v[70:71], v[74:75], v[70:71]
	v_cvt_pk_bf16_f32 v70, v70, v71
	v_cvt_pk_bf16_f32 v71, v68, v69
	global_store_dwordx2 v[234:235], v[70:71], off
	v_lshlrev_b32_e32 v16, 16, v226
	v_and_b32_e32 v17, 0xffff0000, v226
	v_lshlrev_b32_e32 v18, 16, v227
	v_and_b32_e32 v19, 0xffff0000, v227
	v_pk_add_f32 v[20:21], v[144:145], v[198:199] op_sel_hi:[1,0]
	v_pk_add_f32 v[22:23], v[146:147], v[198:199] op_sel_hi:[1,0]
	v_pk_mul_f32 v[20:21], v[20:21], v[16:17]
	v_pk_mul_f32 v[22:23], v[22:23], v[18:19]
	v_cvt_pk_bf16_f32 v20, v20, v21
	s_nop 0
	v_cvt_pk_bf16_f32 v21, v22, v23
	global_store_dwordx2 v[234:235], v[20:21], off offset:32
	s_waitcnt vmcnt(23)
	v_lshlrev_b32_e32 v70, 16, v228
	v_and_b32_e32 v71, 0xffff0000, v228
	v_lshlrev_b32_e32 v68, 16, v229
	v_and_b32_e32 v69, 0xffff0000, v229
	v_pk_add_f32 v[72:73], v[150:151], v[200:201] op_sel_hi:[1,0]
	v_pk_add_f32 v[74:75], v[148:149], v[200:201] op_sel_hi:[1,0]
	v_pk_mul_f32 v[68:69], v[72:73], v[68:69]
	v_pk_mul_f32 v[70:71], v[74:75], v[70:71]
	v_cvt_pk_bf16_f32 v70, v70, v71
	v_cvt_pk_bf16_f32 v71, v68, v69
	global_store_dwordx2 v[236:237], v[70:71], off
	v_lshlrev_b32_e32 v16, 16, v230
	v_and_b32_e32 v17, 0xffff0000, v230
	v_lshlrev_b32_e32 v18, 16, v231
	v_and_b32_e32 v19, 0xffff0000, v231
	v_pk_add_f32 v[20:21], v[152:153], v[200:201] op_sel_hi:[1,0]
	v_pk_add_f32 v[22:23], v[154:155], v[200:201] op_sel_hi:[1,0]
	v_pk_mul_f32 v[20:21], v[20:21], v[16:17]
	v_pk_mul_f32 v[22:23], v[22:23], v[18:19]
	v_cvt_pk_bf16_f32 v20, v20, v21
	s_nop 0
	v_cvt_pk_bf16_f32 v21, v22, v23
	global_store_dwordx2 v[236:237], v[20:21], off offset:32
	s_waitcnt vmcnt(22)
	v_lshlrev_b32_e32 v70, 16, v246
	v_and_b32_e32 v71, 0xffff0000, v246
	v_lshlrev_b32_e32 v68, 16, v247
	v_and_b32_e32 v69, 0xffff0000, v247
	v_pk_add_f32 v[72:73], v[158:159], v[202:203] op_sel_hi:[1,0]
	v_pk_add_f32 v[74:75], v[156:157], v[202:203] op_sel_hi:[1,0]
	v_pk_mul_f32 v[68:69], v[72:73], v[68:69]
	v_pk_mul_f32 v[70:71], v[74:75], v[70:71]
	v_cvt_pk_bf16_f32 v70, v70, v71
	v_cvt_pk_bf16_f32 v71, v68, v69
	global_store_dwordx2 v[238:239], v[70:71], off
	v_lshlrev_b32_e32 v16, 16, v248
	v_and_b32_e32 v17, 0xffff0000, v248
	v_lshlrev_b32_e32 v18, 16, v249
	v_and_b32_e32 v19, 0xffff0000, v249
	v_pk_add_f32 v[20:21], v[160:161], v[202:203] op_sel_hi:[1,0]
	v_pk_add_f32 v[22:23], v[162:163], v[202:203] op_sel_hi:[1,0]
	v_pk_mul_f32 v[20:21], v[20:21], v[16:17]
	v_pk_mul_f32 v[22:23], v[22:23], v[18:19]
	v_cvt_pk_bf16_f32 v20, v20, v21
	s_nop 0
	v_cvt_pk_bf16_f32 v21, v22, v23
	global_store_dwordx2 v[238:239], v[20:21], off offset:32
	s_barrier
	s_branch .LBB0_833
; __device__ __forceinline__ unsigned cvt_pk_bf16(float lo, float hi) { unsigned r; asm volatile("v_cvt_pk_bf16_f32 %0, %1, %2" : "=v"(r) : "v"(lo), "v"(hi)); return r; }
; #define LAS __attribute__((address_space(3)))
; __device__ __forceinline__ void mma_128(const LAS bf16* sA, const LAS bf16* sBt, int wave, int lane, f32x4 (&acc)[4][2]) {
;     ...
;     for (int kk = 0; kk < 4; ++kk) {
;         bf16x8 af[4], bf_[2];
; #pragma unroll
;         for (int mt = 0; mt < 4; ++mt) af[mt] = *(const LAS bf16x8*)(sA + (64 * wm + 16 * mt + fr) * TP + 32 * kk + 8 * fq);
; #pragma unroll
;         for (int nt = 0; nt < 2; ++nt) bf_[nt] = *(const LAS bf16x8*)(sBt + (32 * wn + 16 * nt + fr) * TP + 32 * kk + 8 * fq);
; #pragma unroll
;         for (int mt = 0; mt < 4; ++mt)
; #pragma unroll
;             for (int nt = 0; nt < 2; ++nt) acc[mt][nt] = __builtin_amdgcn_mfma_f32_16x16x32_bf16(bf_[nt], af[mt], acc[mt][nt], 0, 0, 0);
; __device__ __forceinline__ void gmlp_unit(Frame& F, const Args& a, int layer, int unit) {
;     ...
;         mma_128(sA, sB, wave, lane, acc);
;         { const int wm = wave >> 2, wn = wave & 3, fr = lane & 15, fq = lane >> 4;
; #pragma unroll
;           for (int mt = 0; mt < 4; ++mt) { const int tt = 64 * wm + 16 * mt + fr; const float bsv = bsp[g * 128 + tt];
; #pragma unroll
;               for (int nt = 0; nt < 2; ++nt) { const int c = g * 128 + 32 * wn + 16 * nt + 4 * fq;
;                   const v2u uw = *(const v2u*)(GUV + (t0 + tt) * 2048 + c);
;                   const f32x4 u4 = (f32x4){bflo(uw.x), bfhi(uw.x), bflo(uw.y), bfhi(uw.y)};
;                   const f32x4 yb = u4 * (acc[mt][nt] + bsv);
;                   v2u ow; ow.x = cvt_pk_bf16(yb.x, yb.y); ow.y = cvt_pk_bf16(yb.z, yb.w);
;                   *(v2u*)(GUV + (t0 + tt) * 2048 + c) = ow; } } }
;         __syncthreads();
.Lgm_u1_last:
	ds_read_b128 v[2:5], v61 offset:1024
	ds_read_b128 v[6:9], v61 offset:5376
	ds_read_b128 v[10:13], v61 offset:9728
	ds_read_b128 v[14:17], v61 offset:14080
	ds_read_b128 v[18:21], v62 offset:35840
	ds_read_b128 v[22:25], v62 offset:40192
	ds_read_b128 v[84:87], v61 offset:1088
	ds_read_b128 v[88:91], v61 offset:5440
	ds_read_b128 v[92:95], v61 offset:9792
	ds_read_b128 v[96:99], v61 offset:14144
	ds_read_b128 v[76:79], v62 offset:35904
	ds_read_b128 v[80:83], v62 offset:40256
	s_waitcnt lgkmcnt(6)
	v_mfma_f32_16x16x32_bf16 v[132:135], v[18:21], v[2:5], 0
	v_mfma_f32_16x16x32_bf16 v[136:139], v[22:25], v[2:5], 0
	v_mfma_f32_16x16x32_bf16 v[140:143], v[18:21], v[6:9], 0
	v_mfma_f32_16x16x32_bf16 v[144:147], v[22:25], v[6:9], 0
	v_mfma_f32_16x16x32_bf16 v[148:151], v[18:21], v[10:13], 0
	v_mfma_f32_16x16x32_bf16 v[152:155], v[22:25], v[10:13], 0
	v_mfma_f32_16x16x32_bf16 v[156:159], v[18:21], v[14:17], 0
	v_mfma_f32_16x16x32_bf16 v[160:163], v[22:25], v[14:17], 0
	ds_read_b128 v[2:5], v61 offset:1152
	ds_read_b128 v[6:9], v61 offset:5504
	ds_read_b128 v[10:13], v61 offset:9856
	ds_read_b128 v[14:17], v61 offset:14208
	ds_read_b128 v[18:21], v62 offset:35968
	ds_read_b128 v[22:25], v62 offset:40320
	s_waitcnt lgkmcnt(6)
	v_mfma_f32_16x16x32_bf16 v[132:135], v[76:79], v[84:87], v[132:135]
	v_mfma_f32_16x16x32_bf16 v[136:139], v[80:83], v[84:87], v[136:139]
	v_mfma_f32_16x16x32_bf16 v[140:143], v[76:79], v[88:91], v[140:143]
	v_mfma_f32_16x16x32_bf16 v[144:147], v[80:83], v[88:91], v[144:147]
	v_mfma_f32_16x16x32_bf16 v[148:151], v[76:79], v[92:95], v[148:151]
	v_mfma_f32_16x16x32_bf16 v[152:155], v[80:83], v[92:95], v[152:155]
	v_mfma_f32_16x16x32_bf16 v[156:159], v[76:79], v[96:99], v[156:159]
	v_mfma_f32_16x16x32_bf16 v[160:163], v[80:83], v[96:99], v[160:163]
	ds_read_b128 v[84:87], v61 offset:1216
	ds_read_b128 v[88:91], v61 offset:5568
	ds_read_b128 v[92:95], v61 offset:9920
	ds_read_b128 v[96:99], v61 offset:14272
	ds_read_b128 v[76:79], v62 offset:36032
	ds_read_b128 v[80:83], v62 offset:40384
	s_waitcnt lgkmcnt(6)
	v_mfma_f32_16x16x32_bf16 v[132:135], v[18:21], v[2:5], v[132:135]
	v_mfma_f32_16x16x32_bf16 v[136:139], v[22:25], v[2:5], v[136:139]
	v_mfma_f32_16x16x32_bf16 v[140:143], v[18:21], v[6:9], v[140:143]
	v_mfma_f32_16x16x32_bf16 v[144:147], v[22:25], v[6:9], v[144:147]
	v_mfma_f32_16x16x32_bf16 v[148:151], v[18:21], v[10:13], v[148:151]
	v_mfma_f32_16x16x32_bf16 v[152:155], v[22:25], v[10:13], v[152:155]
	v_mfma_f32_16x16x32_bf16 v[156:159], v[18:21], v[14:17], v[156:159]
	v_mfma_f32_16x16x32_bf16 v[160:163], v[22:25], v[14:17], v[160:163]
	s_waitcnt lgkmcnt(0)
	v_mfma_f32_16x16x32_bf16 v[132:135], v[76:79], v[84:87], v[132:135]
	v_mfma_f32_16x16x32_bf16 v[136:139], v[80:83], v[84:87], v[136:139]
	v_mfma_f32_16x16x32_bf16 v[140:143], v[76:79], v[88:91], v[140:143]
	v_mfma_f32_16x16x32_bf16 v[144:147], v[80:83], v[88:91], v[144:147]
	v_mfma_f32_16x16x32_bf16 v[148:151], v[76:79], v[92:95], v[148:151]
	v_mfma_f32_16x16x32_bf16 v[152:155], v[80:83], v[92:95], v[152:155]
	v_mfma_f32_16x16x32_bf16 v[156:159], v[76:79], v[96:99], v[156:159]
	v_mfma_f32_16x16x32_bf16 v[160:163], v[80:83], v[96:99], v[160:163]
	s_nop 7
	s_nop 1
	s_waitcnt vmcnt(9)
	v_lshlrev_b32_e32 v70, 16, v204
	v_and_b32_e32 v71, 0xffff0000, v204
	v_lshlrev_b32_e32 v68, 16, v205
	v_and_b32_e32 v69, 0xffff0000, v205
	v_pk_add_f32 v[72:73], v[134:135], v[196:197] op_sel_hi:[1,0]
	v_pk_add_f32 v[74:75], v[132:133], v[196:197] op_sel_hi:[1,0]
	v_pk_mul_f32 v[68:69], v[72:73], v[68:69]
	v_pk_mul_f32 v[70:71], v[74:75], v[70:71]
	v_cvt_pk_bf16_f32 v70, v70, v71
	v_cvt_pk_bf16_f32 v71, v68, v69
	global_store_dwordx2 v[232:233], v[70:71], off
	v_lshlrev_b32_e32 v16, 16, v206
	v_and_b32_e32 v17, 0xffff0000, v206
	v_lshlrev_b32_e32 v18, 16, v207
	v_and_b32_e32 v19, 0xffff0000, v207
	v_pk_add_f32 v[20:21], v[136:137], v[196:197] op_sel_hi:[1,0]
	v_pk_add_f32 v[22:23], v[138:139], v[196:197] op_sel_hi:[1,0]
	v_pk_mul_f32 v[20:21], v[20:21], v[16:17]
	v_pk_mul_f32 v[22:23], v[22:23], v[18:19]
	v_cvt_pk_bf16_f32 v20, v20, v21
	s_nop 0
	v_cvt_pk_bf16_f32 v21, v22, v23
	global_store_dwordx2 v[232:233], v[20:21], off offset:32
	s_waitcnt vmcnt(8)
	v_lshlrev_b32_e32 v70, 16, v224
	v_and_b32_e32 v71, 0xffff0000, v224
	v_lshlrev_b32_e32 v68, 16, v225
	v_and_b32_e32 v69, 0xffff0000, v225
	v_pk_add_f32 v[72:73], v[142:143], v[198:199] op_sel_hi:[1,0]
	v_pk_add_f32 v[74:75], v[140:141], v[198:199] op_sel_hi:[1,0]
	v_pk_mul_f32 v[68:69], v[72:73], v[68:69]
	v_pk_mul_f32 v[70:71], v[74:75], v[70:71]
	v_cvt_pk_bf16_f32 v70, v70, v71
	v_cvt_pk_bf16_f32 v71, v68, v69
	global_store_dwordx2 v[234:235], v[70:71], off
	v_lshlrev_b32_e32 v16, 16, v226
	v_and_b32_e32 v17, 0xffff0000, v226
	v_lshlrev_b32_e32 v18, 16, v227
	v_and_b32_e32 v19, 0xffff0000, v227
	v_pk_add_f32 v[20:21], v[144:145], v[198:199] op_sel_hi:[1,0]
	v_pk_add_f32 v[22:23], v[146:147], v[198:199] op_sel_hi:[1,0]
	v_pk_mul_f32 v[20:21], v[20:21], v[16:17]
	v_pk_mul_f32 v[22:23], v[22:23], v[18:19]
	v_cvt_pk_bf16_f32 v20, v20, v21
	s_nop 0
	v_cvt_pk_bf16_f32 v21, v22, v23
	global_store_dwordx2 v[234:235], v[20:21], off offset:32
	s_waitcnt vmcnt(7)
; __device__ __forceinline__ unsigned cvt_pk_bf16(float lo, float hi) { unsigned r; asm volatile("v_cvt_pk_bf16_f32 %0, %1, %2" : "=v"(r) : "v"(lo), "v"(hi)); return r; }
; __device__ __forceinline__ void gmlp_unit(Frame& F, const Args& a, int layer, int unit) {
;     ...
;         { const int wm = wave >> 2, wn = wave & 3, fr = lane & 15, fq = lane >> 4;
; #pragma unroll
;           for (int mt = 0; mt < 4; ++mt) { const int tt = 64 * wm + 16 * mt + fr; const float bsv = bsp[g * 128 + tt];
; #pragma unroll
;               for (int nt = 0; nt < 2; ++nt) { const int c = g * 128 + 32 * wn + 16 * nt + 4 * fq;
;                   const v2u uw = *(const v2u*)(GUV + (t0 + tt) * 2048 + c);
;                   const f32x4 u4 = (f32x4){bflo(uw.x), bfhi(uw.x), bflo(uw.y), bfhi(uw.y)};
;                   const f32x4 yb = u4 * (acc[mt][nt] + bsv);
;                   v2u ow; ow.x = cvt_pk_bf16(yb.x, yb.y); ow.y = cvt_pk_bf16(yb.z, yb.w);
;                   *(v2u*)(GUV + (t0 + tt) * 2048 + c) = ow; } } }
;         __syncthreads();
	v_lshlrev_b32_e32 v70, 16, v228
	v_and_b32_e32 v71, 0xffff0000, v228
	v_lshlrev_b32_e32 v68, 16, v229
	v_and_b32_e32 v69, 0xffff0000, v229
	v_pk_add_f32 v[72:73], v[150:151], v[200:201] op_sel_hi:[1,0]
	v_pk_add_f32 v[74:75], v[148:149], v[200:201] op_sel_hi:[1,0]
	v_pk_mul_f32 v[68:69], v[72:73], v[68:69]
	v_pk_mul_f32 v[70:71], v[74:75], v[70:71]
	v_cvt_pk_bf16_f32 v70, v70, v71
	v_cvt_pk_bf16_f32 v71, v68, v69
	global_store_dwordx2 v[236:237], v[70:71], off
	v_lshlrev_b32_e32 v16, 16, v230
	v_and_b32_e32 v17, 0xffff0000, v230
	v_lshlrev_b32_e32 v18, 16, v231
	v_and_b32_e32 v19, 0xffff0000, v231
	v_pk_add_f32 v[20:21], v[152:153], v[200:201] op_sel_hi:[1,0]
	v_pk_add_f32 v[22:23], v[154:155], v[200:201] op_sel_hi:[1,0]
	v_pk_mul_f32 v[20:21], v[20:21], v[16:17]
	v_pk_mul_f32 v[22:23], v[22:23], v[18:19]
	v_cvt_pk_bf16_f32 v20, v20, v21
	s_nop 0
	v_cvt_pk_bf16_f32 v21, v22, v23
	global_store_dwordx2 v[236:237], v[20:21], off offset:32
	s_waitcnt vmcnt(6)
	v_lshlrev_b32_e32 v70, 16, v246
	v_and_b32_e32 v71, 0xffff0000, v246
	v_lshlrev_b32_e32 v68, 16, v247
	v_and_b32_e32 v69, 0xffff0000, v247
	v_pk_add_f32 v[72:73], v[158:159], v[202:203] op_sel_hi:[1,0]
	v_pk_add_f32 v[74:75], v[156:157], v[202:203] op_sel_hi:[1,0]
	v_pk_mul_f32 v[68:69], v[72:73], v[68:69]
	v_pk_mul_f32 v[70:71], v[74:75], v[70:71]
	v_cvt_pk_bf16_f32 v70, v70, v71
	v_cvt_pk_bf16_f32 v71, v68, v69
	global_store_dwordx2 v[238:239], v[70:71], off
	v_lshlrev_b32_e32 v16, 16, v248
	v_and_b32_e32 v17, 0xffff0000, v248
	v_lshlrev_b32_e32 v18, 16, v249
	v_and_b32_e32 v19, 0xffff0000, v249
	v_pk_add_f32 v[20:21], v[160:161], v[202:203] op_sel_hi:[1,0]
	v_pk_add_f32 v[22:23], v[162:163], v[202:203] op_sel_hi:[1,0]
	v_pk_mul_f32 v[20:21], v[20:21], v[16:17]
	v_pk_mul_f32 v[22:23], v[22:23], v[18:19]
	v_cvt_pk_bf16_f32 v20, v20, v21
	s_nop 0
	v_cvt_pk_bf16_f32 v21, v22, v23
	global_store_dwordx2 v[238:239], v[20:21], off offset:32
	s_barrier
; __device__ __forceinline__ void unpk8(const u32x4 w, f32x4& a, f32x4& b) { a = (f32x4){bflo(w.x), bfhi(w.x), bflo(w.y), bfhi(w.y)}; b = (f32x4){bflo(w.z), bfhi(w.z), bflo(w.w), bfhi(w.w)}; }
; __device__ __forceinline__ void gmlp_unit(Frame& F, const Args& a, int layer, int unit) {
;     ...
;     for (int r = 0; r < 16; ++r) { const int tok = wave * 16 + r; const bf16* rowp = GUV + (t0 + tok) * 2048 + 1024;
;         f32x4 x0, x1, x2, x3; unpk8(*(const v4u*)(rowp + lane * 8), x0, x1); unpk8(*(const v4u*)(rowp + 512 + lane * 8), x2, x3);
;         const f32x4 sv = (x0 + x1) + (x2 + x3), qv = (x0 * x0 + x1 * x1) + (x2 * x2 + x3 * x3);
;         const float s = wave_sum((sv.x + sv.y) + (sv.z + sv.w)), q = wave_sum((qv.x + qv.y) + (qv.z + qv.w));
;         const float mean = s * (1.f / 1024.f), var = fmaxf(q * (1.f / 1024.f) - mean * mean, 0.f);
;         if (lane == 0) { st[tok * 2] = mean; st[tok * 2 + 1] = 1.f / sqrtf(var + 1e-5f); } }
	s_ashr_i32 s3, s2, 31
	s_lshl_b64 s[36:37], s[2:3], 19
	v_readlane_b32 s21, v254, 19
	v_mbcnt_lo_u32_b32 v6, -1, 0
	v_mbcnt_hi_u32_b32 v6, -1, v6
	s_add_u32 s21, s6, s21
	v_readlane_b32 s23, v254, 20
	s_addc_u32 s23, s7, s23
	v_lshlrev_b32_e32 v2, 3, v6
	s_add_u32 s38, s21, s36
	v_ashrrev_i32_e32 v3, 31, v2
	s_addc_u32 s39, s23, s37
	s_mov_b32 s3, 0
	v_cmp_eq_u32_e64 s[42:43], 0, v6
	v_lshl_add_u64 v[4:5], v[2:3], 1, s[38:39]
	global_load_dwordx4 v[32:35], v[4:5], off
	global_load_dwordx4 v[36:39], v[4:5], off offset:1024
	v_lshl_add_u64 v[4:5], v[4:5], 0, s[78:79]
	global_load_dwordx4 v[40:43], v[4:5], off
	global_load_dwordx4 v[44:47], v[4:5], off offset:1024
	v_lshl_add_u64 v[4:5], v[4:5], 0, s[78:79]
	global_load_dwordx4 v[48:51], v[4:5], off
	global_load_dwordx4 v[52:55], v[4:5], off offset:1024
	v_lshl_add_u64 v[4:5], v[4:5], 0, s[78:79]
	global_load_dwordx4 v[56:59], v[4:5], off
	global_load_dwordx4 v[60:63], v[4:5], off offset:1024
	v_lshl_add_u64 v[4:5], v[4:5], 0, s[78:79]
	global_load_dwordx4 v[64:67], v[4:5], off
	global_load_dwordx4 v[68:71], v[4:5], off offset:1024
	v_lshl_add_u64 v[4:5], v[4:5], 0, s[78:79]
	global_load_dwordx4 v[72:75], v[4:5], off
	global_load_dwordx4 v[76:79], v[4:5], off offset:1024
	v_lshl_add_u64 v[4:5], v[4:5], 0, s[78:79]
	global_load_dwordx4 v[80:83], v[4:5], off
	global_load_dwordx4 v[84:87], v[4:5], off offset:1024
	v_lshl_add_u64 v[4:5], v[4:5], 0, s[78:79]
	global_load_dwordx4 v[88:91], v[4:5], off
	global_load_dwordx4 v[92:95], v[4:5], off offset:1024
	v_lshl_add_u64 v[4:5], v[4:5], 0, s[78:79]
	global_load_dwordx4 v[100:103], v[4:5], off
	global_load_dwordx4 v[104:107], v[4:5], off offset:1024
	v_lshl_add_u64 v[4:5], v[4:5], 0, s[78:79]
	global_load_dwordx4 v[108:111], v[4:5], off
	global_load_dwordx4 v[112:115], v[4:5], off offset:1024
	v_lshl_add_u64 v[4:5], v[4:5], 0, s[78:79]
	global_load_dwordx4 v[116:119], v[4:5], off
	global_load_dwordx4 v[120:123], v[4:5], off offset:1024
	v_lshl_add_u64 v[4:5], v[4:5], 0, s[78:79]
	global_load_dwordx4 v[124:127], v[4:5], off
	global_load_dwordx4 v[128:131], v[4:5], off offset:1024
	v_lshl_add_u64 v[4:5], v[4:5], 0, s[78:79]
	global_load_dwordx4 v[132:135], v[4:5], off
	global_load_dwordx4 v[136:139], v[4:5], off offset:1024
	v_lshl_add_u64 v[4:5], v[4:5], 0, s[78:79]
	global_load_dwordx4 v[140:143], v[4:5], off
	global_load_dwordx4 v[144:147], v[4:5], off offset:1024
	v_lshl_add_u64 v[4:5], v[4:5], 0, s[78:79]
	global_load_dwordx4 v[148:151], v[4:5], off
	global_load_dwordx4 v[152:155], v[4:5], off offset:1024
	v_lshl_add_u64 v[4:5], v[4:5], 0, s[78:79]
	global_load_dwordx4 v[156:159], v[4:5], off
	global_load_dwordx4 v[160:163], v[4:5], off offset:1024
	v_lshl_add_u64 v[4:5], v[4:5], 0, s[78:79]
	s_waitcnt vmcnt(30)
	v_lshlrev_b32_e32 v16, 16, v32
	v_and_b32_e32 v17, 0xffff0000, v32
	v_lshlrev_b32_e32 v8, 16, v33
	v_and_b32_e32 v9, 0xffff0000, v33
	v_lshlrev_b32_e32 v18, 16, v34
	v_and_b32_e32 v19, 0xffff0000, v34
	v_lshlrev_b32_e32 v10, 16, v35
	v_and_b32_e32 v11, 0xffff0000, v35
	v_lshlrev_b32_e32 v20, 16, v36
	v_and_b32_e32 v21, 0xffff0000, v36
	v_lshlrev_b32_e32 v12, 16, v37
	v_and_b32_e32 v13, 0xffff0000, v37
	v_lshlrev_b32_e32 v22, 16, v38
	v_and_b32_e32 v23, 0xffff0000, v38
	v_lshlrev_b32_e32 v14, 16, v39
	v_and_b32_e32 v15, 0xffff0000, v39
	v_pk_add_f32 v[24:25], v[16:17], v[18:19]
	v_pk_add_f32 v[26:27], v[8:9], v[10:11]
	v_pk_add_f32 v[28:29], v[20:21], v[22:23]
	v_pk_add_f32 v[30:31], v[12:13], v[14:15]
	v_pk_mul_f32 v[10:11], v[10:11], v[10:11]
	v_pk_mul_f32 v[18:19], v[18:19], v[18:19]
	v_pk_mul_f32 v[14:15], v[14:15], v[14:15]
	v_pk_mul_f32 v[22:23], v[22:23], v[22:23]
	v_pk_add_f32 v[26:27], v[26:27], v[30:31]
	v_pk_add_f32 v[24:25], v[24:25], v[28:29]
	v_pk_fma_f32 v[16:17], v[16:17], v[16:17], v[18:19]
	v_pk_fma_f32 v[8:9], v[8:9], v[8:9], v[10:11]
	v_pk_fma_f32 v[10:11], v[20:21], v[20:21], v[22:23]
	v_pk_fma_f32 v[12:13], v[12:13], v[12:13], v[14:15]
	v_pk_add_f32 v[10:11], v[16:17], v[10:11]
	v_pk_add_f32 v[8:9], v[8:9], v[12:13]
	v_add_f32_e32 v1, v24, v25
	v_add_f32_e32 v3, v26, v27
	v_add_f32_e32 v1, v1, v3
	v_add_f32_e32 v3, v10, v11
	v_add_f32_e32 v7, v8, v9
	v_add_f32_e32 v3, v3, v7
	v_add_f32_dpp v1, v1, v1 quad_perm:[1,0,3,2] row_mask:0xf bank_mask:0xf bound_ctrl:1
	s_nop 0
	v_add_f32_dpp v3, v3, v3 quad_perm:[1,0,3,2] row_mask:0xf bank_mask:0xf bound_ctrl:1
	v_add_f32_dpp v1, v1, v1 quad_perm:[2,3,0,1] row_mask:0xf bank_mask:0xf bound_ctrl:1
	s_nop 0
	v_add_f32_dpp v3, v3, v3 quad_perm:[2,3,0,1] row_mask:0xf bank_mask:0xf bound_ctrl:1
	v_add_f32_dpp v1, v1, v1 row_half_mirror row_mask:0xf bank_mask:0xf bound_ctrl:1
	s_nop 0
	v_add_f32_dpp v3, v3, v3 row_half_mirror row_mask:0xf bank_mask:0xf bound_ctrl:1
	v_add_f32_dpp v1, v1, v1 row_mirror row_mask:0xf bank_mask:0xf bound_ctrl:1
	v_mov_b32_e32 v7, v1
	v_add_f32_dpp v8, v3, v3 row_mirror row_mask:0xf bank_mask:0xf bound_ctrl:1
	v_mov_b32_e32 v9, v8
	v_permlane16_swap_b32_e32 v1, v7
	s_nop 0
	v_permlane16_swap_b32_e32 v8, v9
	v_add_f32_e32 v1, v1, v7
	v_add_f32_e32 v7, v8, v9
	v_mov_b32_e32 v3, v1
	v_mov_b32_e32 v8, v7
	s_nop 0
	v_permlane32_swap_b32_e32 v1, v3
	v_permlane32_swap_b32_e32 v7, v8
	s_and_saveexec_b64 s[38:39], s[42:43]
	s_cbranch_execz .Lgm_u2_st0
	v_add_f32_e32 v1, v1, v3
	v_add_f32_e32 v7, v7, v8
	v_mul_f32_e32 v8, 0x3a800000, v1
	v_mul_f32_e32 v1, v8, v8
	v_fma_f32 v1, v7, s13, -v1
	v_max_f32_e32 v1, 0, v1
	v_add_f32_e32 v1, 0x3727c5ac, v1
	v_mul_f32_e32 v3, 0x4f800000, v1
	v_cmp_gt_f32_e32 vcc, s69, v1
	s_add_i32 s21, s11, s3
	s_nop 0
	v_cndmask_b32_e32 v1, v1, v3, vcc
	v_sqrt_f32_e32 v3, v1
	s_nop 0
	v_add_u32_e32 v7, -1, v3
	v_fma_f32 v9, -v7, v3, v1
	v_cmp_ge_f32_e64 s[44:45], 0, v9
	v_add_u32_e32 v9, 1, v3
	s_nop 0
	v_cndmask_b32_e64 v7, v3, v7, s[44:45]
	v_fma_f32 v3, -v9, v3, v1
	v_cmp_lt_f32_e64 s[44:45], 0, v3
	s_nop 1
	v_cndmask_b32_e64 v3, v7, v9, s[44:45]
	v_mul_f32_e32 v7, 0x37800000, v3
	v_cndmask_b32_e32 v3, v3, v7, vcc
	v_cmp_class_f32_e32 vcc, v1, v242
	s_nop 1
	v_cndmask_b32_e32 v1, v3, v1, vcc
	v_div_scale_f32 v3, s[44:45], v1, v1, 1.0
	v_rcp_f32_e32 v7, v3
	s_nop 0
	v_fma_f32 v9, -v3, v7, 1.0
	v_fmac_f32_e32 v7, v9, v7
	v_div_scale_f32 v9, vcc, 1.0, v1, 1.0
	v_mul_f32_e32 v10, v9, v7
	v_fma_f32 v11, -v3, v10, v9
	v_fmac_f32_e32 v10, v11, v7
	v_fma_f32 v3, -v3, v10, v9
	v_div_fmas_f32 v3, v3, v7, v10
	v_div_fixup_f32 v9, v3, v1, 1.0
	v_mov_b32_e32 v1, s21
	ds_write_b64 v1, v[8:9]

; __device__ __forceinline__ void unpk8(const u32x4 w, f32x4& a, f32x4& b) { a = (f32x4){bflo(w.x), bfhi(w.x), bflo(w.y), bfhi(w.y)}; b = (f32x4){bflo(w.z), bfhi(w.z), bflo(w.w), bfhi(w.w)}; }
; #define LAS __attribute__((address_space(3)))
; __device__ __forceinline__ void gmlp_unit(Frame& F, const Args& a, int layer, int unit) {
;     ...
;     for (int g = 0; g < 8; ++g) {
; #pragma unroll
;         for (int i = 0; i < 4; ++i) { const int pc = tid + 512 * i, rr = pc >> 4, c16 = pc & 15;
;             *(LAS v4u*)(sA + rr * TP + c16 * 8) = *(const v4u*)(GMW + (size_t)g * 16384 + rr * 128 + c16 * 8); }
;         { const int p = tid & 127, oc0 = tid >> 7; const float mean = st[p * 2], rstd = st[p * 2 + 1];
; #pragma unroll
;           for (int i = 0; i < 4; ++i) { const int oc = oc0 + 4 * i, c0 = g * 128 + oc * 8;
;               f32x4 x0, x1; unpk8(*(const v4u*)(GUV + (t0 + p) * 2048 + 1024 + c0), x0, x1);
;               const f32x4 g0 = *(const f32x4*)(lng + c0), g1 = *(const f32x4*)(lng + c0 + 4), b0 = *(const f32x4*)(lnb + c0), b1 = *(const f32x4*)(lnb + c0 + 4);
.LBB0_838:
	s_or_b32 s22, s22, 1
	v_and_b32_e32 v19, 15, v6
	v_and_b32_e32 v4, -16, v6
	s_ashr_i32 s23, s22, 31
	v_add_u32_e32 v3, s27, v6
	v_add_u32_e32 v20, 0, v4
	v_or_b32_e32 v7, s75, v19
	v_or_b32_e32 v4, s77, v19
	v_ashrrev_i32_e32 v6, 2, v6
	s_lshl_b64 s[22:23], s[22:23], 7
	v_mul_u32_u24_e32 v22, 0x110, v7
	v_and_b32_e32 v23, -4, v6
	v_or_b32_e32 v6, 48, v4
	v_mov_b32_e32 v7, v0
	s_add_u32 s38, s6, 0x28400000
	v_lshl_add_u64 v[6:7], s[22:23], 0, v[6:7]
	s_addc_u32 s39, s7, 0
	v_ashrrev_i32_e32 v5, 4, v3
	s_movk_i32 s3, 0x110
	v_lshlrev_b64 v[6:7], 12, v[6:7]
	v_and_b32_e32 v1, 0x78, v2
	v_and_b32_e32 v2, -8, v5
	v_lshl_add_u64 v[26:27], s[38:39], 0, v[6:7]
	v_lshlrev_b32_e32 v6, 7, v5
	v_mul_lo_u32 v24, v5, s3
	v_add_u32_e32 v5, 0x200, v3
	v_ashrrev_i32_e32 v5, 4, v5
	v_lshlrev_b32_e32 v8, 7, v5
	v_mul_lo_u32 v25, v5, s3
	v_add_u32_e32 v5, 0x400, v3
	v_ashrrev_i32_e32 v5, 4, v5
	v_lshlrev_b32_e32 v10, 7, v5
	v_mul_lo_u32 v41, v5, s3
	v_mov_b32_e32 v5, v0
	v_lshl_add_u64 v[14:15], s[22:23], 0, v[4:5]
	v_lshlrev_b64 v[14:15], 12, v[14:15]
	v_mul_lo_u32 v21, v4, s3
	v_lshl_add_u64 v[28:29], s[38:39], 0, v[14:15]
	v_or_b32_e32 v14, 16, v4
	v_or_b32_e32 v4, 32, v4
	v_lshl_add_u64 v[4:5], s[22:23], 0, v[4:5]
	v_lshlrev_b64 v[4:5], 12, v[4:5]
	v_lshl_add_u64 v[32:33], s[38:39], 0, v[4:5]
	v_lshlrev_b32_e32 v4, 4, v19
	v_mov_b32_e32 v5, v0
	v_ashrrev_i32_e32 v7, 31, v6
	v_mov_b32_e32 v15, v0
	v_lshl_add_u64 v[4:5], s[0:1], 0, v[4:5]
	v_readlane_b32 s40, v251, 34
	v_and_b32_e32 v17, 0x7f, v3
	v_add_u32_e32 v3, 0x600, v3
	v_lshl_add_u64 v[14:15], s[22:23], 0, v[14:15]
	v_lshl_add_u64 v[34:35], v[6:7], 1, v[4:5]
	v_add_u32_e32 v6, s77, v19
	v_mov_b32_e32 v7, v0
	v_readlane_b32 s52, v251, 46
	v_readlane_b32 s53, v251, 47
	s_add_u32 s22, s36, 0x28400880
	v_ashrrev_i32_e32 v3, 4, v3
	v_lshl_add_u64 v[38:39], v[6:7], 2, s[52:53]
	s_addc_u32 s23, s37, 0
	v_lshlrev_b32_e32 v6, 12, v17
	v_lshl_add_u32 v16, v1, 1, 0
	v_lshl_add_u32 v1, v17, 3, 0
	v_lshlrev_b32_e32 v12, 7, v3
	v_mul_lo_u32 v52, v3, s3
	v_lshl_add_u64 v[6:7], s[22:23], 0, v[6:7]
	v_ashrrev_i32_e32 v3, 31, v2
	v_mad_i32_i24 v18, v17, -6, v1
	v_ashrrev_i32_e32 v9, 31, v8
	v_ashrrev_i32_e32 v11, 31, v10
	v_ashrrev_i32_e32 v13, 31, v12
	v_mul_lo_u32 v53, v2, s3
	v_lshlrev_b64 v[14:15], 12, v[14:15]
	v_readlane_b32 s46, v251, 40
	v_readlane_b32 s47, v251, 41
	v_readlane_b32 s48, v251, 42
	v_readlane_b32 s49, v251, 43
	v_lshl_add_u64 v[44:45], v[2:3], 1, v[6:7]
	v_lshlrev_b64 v[2:3], 2, v[2:3]
	v_lshl_add_u64 v[30:31], s[38:39], 0, v[14:15]
	v_lshl_add_u64 v[36:37], v[8:9], 1, v[4:5]
	v_add_u32_e32 v40, s75, v23
	v_lshl_add_u64 v[42:43], v[10:11], 1, v[4:5]
	v_lshl_add_u64 v[46:47], v[12:13], 1, v[4:5]
	v_lshl_add_u64 v[48:49], s[48:49], 0, v[2:3]
	v_lshl_add_u64 v[50:51], s[46:47], 0, v[2:3]
	s_mov_b64 s[22:23], 0
	v_add_u32_e32 v56, v16, v24
	v_add_u32_e32 v57, v16, v25
	v_add_u32_e32 v58, v16, v41
	v_add_u32_e32 v59, v16, v52
	v_add_u32_e32 v60, v18, v53
	v_add_u32_e32 v61, v20, v21
	v_add_u32_e32 v62, v20, v22
	s_waitcnt lgkmcnt(0)
	s_barrier
	v_readlane_b32 s41, v251, 35
	v_readlane_b32 s42, v251, 36
	v_readlane_b32 s43, v251, 37
	v_readlane_b32 s44, v251, 38
	v_readlane_b32 s45, v251, 39
	v_readlane_b32 s50, v251, 44
	v_readlane_b32 s51, v251, 45
	v_readlane_b32 s54, v251, 48
	v_readlane_b32 s55, v251, 49
	v_lshl_add_u64 v[2:3], s[6:7], 0, v[34:35]
	global_load_dwordx4 v[100:103], v[2:3], off
	v_lshl_add_u64 v[34:35], v[34:35], 0, s[34:35]
	v_lshl_add_u64 v[2:3], s[6:7], 0, v[36:37]
	global_load_dwordx4 v[104:107], v[2:3], off
	v_lshl_add_u64 v[36:37], v[36:37], 0, s[34:35]
	v_lshl_add_u64 v[2:3], s[6:7], 0, v[42:43]
	global_load_dwordx4 v[108:111], v[2:3], off
	v_lshl_add_u64 v[42:43], v[42:43], 0, s[34:35]
	v_lshl_add_u64 v[2:3], s[6:7], 0, v[46:47]
	global_load_dwordx4 v[112:115], v[2:3], off
	v_lshl_add_u64 v[46:47], v[46:47], 0, s[34:35]
	v_lshl_add_u64 v[4:5], s[6:7], 0, v[44:45]
	v_lshl_add_u64 v[6:7], v[48:49], 0, s[22:23]
	v_lshl_add_u64 v[44:45], v[44:45], 0, s[66:67]
	global_load_dwordx4 v[116:119], v[4:5], off offset:-128
	global_load_dwordx4 v[120:123], v[4:5], off offset:-64
	global_load_dwordx4 v[124:127], v[4:5], off
	global_load_dwordx4 v[128:131], v[4:5], off offset:64
	global_load_dwordx4 v[164:167], v[6:7], off
	global_load_dwordx4 v[168:171], v[6:7], off offset:16
	global_load_dwordx4 v[172:175], v[6:7], off offset:128
	global_load_dwordx4 v[176:179], v[6:7], off offset:144
	global_load_dwordx4 v[180:183], v[6:7], off offset:256
	global_load_dwordx4 v[184:187], v[6:7], off offset:272
	global_load_dwordx4 v[188:191], v[6:7], off offset:384
	global_load_dwordx4 v[192:195], v[6:7], off offset:400
; __device__ __forceinline__ void unpk8(const u32x4 w, f32x4& a, f32x4& b) { a = (f32x4){bflo(w.x), bfhi(w.x), bflo(w.y), bfhi(w.y)}; b = (f32x4){bflo(w.z), bfhi(w.z), bflo(w.w), bfhi(w.w)}; }
; __device__ __forceinline__ u32x4 pk8(const f32x4 a, const f32x4 b) { u32x4 w; w.x = cvt_pk_bf16(a[0], a[1]); w.y = cvt_pk_bf16(a[2], a[3]); w.z = cvt_pk_bf16(b[0], b[1]); w.w = cvt_pk_bf16(b[2], b[3]); return w; }
; #define LAS __attribute__((address_space(3)))
; __device__ __forceinline__ void gmlp_unit(Frame& F, const Args& a, int layer, int unit) {
;     ...
;         for (int i = 0; i < 4; ++i) { const int pc = tid + 512 * i, rr = pc >> 4, c16 = pc & 15;
;             *(LAS v4u*)(sA + rr * TP + c16 * 8) = *(const v4u*)(GMW + (size_t)g * 16384 + rr * 128 + c16 * 8); }
;         { const int p = tid & 127, oc0 = tid >> 7; const float mean = st[p * 2], rstd = st[p * 2 + 1];
; #pragma unroll
;           for (int i = 0; i < 4; ++i) { const int oc = oc0 + 4 * i, c0 = g * 128 + oc * 8;
;               f32x4 x0, x1; unpk8(*(const v4u*)(GUV + (t0 + p) * 2048 + 1024 + c0), x0, x1);
;               const f32x4 g0 = *(const f32x4*)(lng + c0), g1 = *(const f32x4*)(lng + c0 + 4), b0 = *(const f32x4*)(lnb + c0), b1 = *(const f32x4*)(lnb + c0 + 4);
;               x0 = (x0 - mean) * rstd * g0 + b0; x1 = (x1 - mean) * rstd * g1 + b1;
;               const v4u w = pk8(x0, x1);
;               LAS bf16* d = sB + (oc * 8) * TP + p;
;               d[0 * TP] = (bf16)(w.x & 0xffffu); d[1 * TP] = (bf16)(w.x >> 16); d[2 * TP] = (bf16)(w.y & 0xffffu); d[3 * TP] = (bf16)(w.y >> 16);
;               d[4 * TP] = (bf16)(w.z & 0xffffu); d[5 * TP] = (bf16)(w.z >> 16); d[6 * TP] = (bf16)(w.w & 0xffffu); d[7 * TP] = (bf16)(w.w >> 16); } }
.LBB0_839:
	ds_read_b64 v[2:3], v1
	v_ashrrev_i32_e32 v41, 31, v40
	v_lshl_add_u64 v[54:55], v[38:39], 0, s[22:23]
	v_lshlrev_b64 v[52:53], 1, v[40:41]
	v_add_u32_e32 v40, 0x80, v40
	v_lshl_add_u64 v[232:233], v[28:29], 0, v[52:53]
	v_lshl_add_u64 v[234:235], v[30:31], 0, v[52:53]
	v_lshl_add_u64 v[236:237], v[32:33], 0, v[52:53]
	v_lshl_add_u64 v[238:239], v[26:27], 0, v[52:53]
	v_lshl_add_u64 v[8:9], v[50:51], 0, s[22:23]
	global_load_dwordx4 v[132:135], v[8:9], off
	global_load_dwordx4 v[136:139], v[8:9], off offset:16
	global_load_dwordx4 v[140:143], v[8:9], off offset:128
	global_load_dwordx4 v[144:147], v[8:9], off offset:144
	global_load_dwordx4 v[148:151], v[8:9], off offset:256
	global_load_dwordx4 v[152:155], v[8:9], off offset:272
	global_load_dwordx4 v[156:159], v[8:9], off offset:384
	global_load_dwordx4 v[160:163], v[8:9], off offset:400
	global_load_dword v196, v[54:55], off
	global_load_dwordx2 v[204:205], v[232:233], off
	global_load_dwordx2 v[206:207], v[232:233], off offset:32
	global_load_dword v198, v[54:55], off offset:64
	global_load_dwordx2 v[224:225], v[234:235], off
	global_load_dwordx2 v[226:227], v[234:235], off offset:32
	global_load_dword v200, v[54:55], off offset:128
	global_load_dwordx2 v[228:229], v[236:237], off
	global_load_dwordx2 v[230:231], v[236:237], off offset:32
	global_load_dword v202, v[54:55], off offset:192
	global_load_dwordx2 v[246:247], v[238:239], off
	global_load_dwordx2 v[248:249], v[238:239], off offset:32
	s_waitcnt vmcnt(35)
	ds_write_b128 v56, v[100:103] offset:1024
	s_waitcnt vmcnt(34)
	ds_write_b128 v57, v[104:107] offset:1024
	s_waitcnt vmcnt(33)
	ds_write_b128 v58, v[108:111] offset:1024
	s_waitcnt vmcnt(32)
	ds_write_b128 v59, v[112:115] offset:1024
	s_waitcnt lgkmcnt(4)
	s_waitcnt vmcnt(18)
	v_lshlrev_b32_e32 v41, 16, v116
	v_and_b32_e32 v54, 0xffff0000, v116
	v_lshlrev_b32_e32 v52, 16, v117
	v_and_b32_e32 v53, 0xffff0000, v117
	v_lshlrev_b32_e32 v63, 16, v118
	v_and_b32_e32 v64, 0xffff0000, v118
	v_lshlrev_b32_e32 v65, 16, v119
	v_and_b32_e32 v66, 0xffff0000, v119
	v_sub_f32_e32 v53, v53, v2
	v_sub_f32_e32 v52, v52, v2
	v_sub_f32_e32 v55, v54, v2
	v_sub_f32_e32 v54, v41, v2
	v_pk_mul_f32 v[52:53], v[2:3], v[52:53] op_sel:[1,0]
	v_pk_mul_f32 v[54:55], v[2:3], v[54:55] op_sel:[1,0]
	v_pk_fma_f32 v[134:135], v[134:135], v[52:53], v[166:167]
	v_sub_f32_e32 v167, v64, v2
	v_sub_f32_e32 v166, v63, v2
	v_pk_fma_f32 v[132:133], v[132:133], v[54:55], v[164:165]
	v_sub_f32_e32 v165, v66, v2
	v_sub_f32_e32 v164, v65, v2
	v_pk_mul_f32 v[166:167], v[2:3], v[166:167] op_sel:[1,0]
	v_pk_mul_f32 v[164:165], v[2:3], v[164:165] op_sel:[1,0]
	v_pk_fma_f32 v[136:137], v[136:137], v[166:167], v[168:169]
	v_cvt_pk_bf16_f32 v132, v132, v133
	v_pk_fma_f32 v[138:139], v[138:139], v[164:165], v[170:171]
	v_cvt_pk_bf16_f32 v133, v134, v135
	v_cvt_pk_bf16_f32 v136, v136, v137
	s_nop 0
	v_cvt_pk_bf16_f32 v137, v138, v139
	ds_write_b16 v60, v132 offset:35840
	ds_write_b16_d16_hi v60, v132 offset:36112
	ds_write_b16 v60, v133 offset:36384
	ds_write_b16_d16_hi v60, v133 offset:36656
	ds_write_b16 v60, v136 offset:36928
	ds_write_b16_d16_hi v60, v136 offset:37200
	ds_write_b16 v60, v137 offset:37472
	ds_write_b16_d16_hi v60, v137 offset:37744
	s_waitcnt vmcnt(16)
	v_lshlrev_b32_e32 v41, 16, v120
	v_and_b32_e32 v54, 0xffff0000, v120
	v_lshlrev_b32_e32 v52, 16, v121
	v_and_b32_e32 v53, 0xffff0000, v121
	v_lshlrev_b32_e32 v63, 16, v122
	v_and_b32_e32 v64, 0xffff0000, v122
	v_lshlrev_b32_e32 v65, 16, v123
	v_and_b32_e32 v66, 0xffff0000, v123
	v_sub_f32_e32 v53, v53, v2
	v_sub_f32_e32 v52, v52, v2
	v_sub_f32_e32 v55, v54, v2
	v_sub_f32_e32 v54, v41, v2
	v_pk_mul_f32 v[52:53], v[2:3], v[52:53] op_sel:[1,0]
	v_pk_mul_f32 v[54:55], v[2:3], v[54:55] op_sel:[1,0]
	v_pk_fma_f32 v[142:143], v[142:143], v[52:53], v[174:175]
	v_sub_f32_e32 v175, v64, v2
	v_sub_f32_e32 v174, v63, v2
	v_pk_fma_f32 v[140:141], v[140:141], v[54:55], v[172:173]
	v_sub_f32_e32 v173, v66, v2
	v_sub_f32_e32 v172, v65, v2
	v_pk_mul_f32 v[174:175], v[2:3], v[174:175] op_sel:[1,0]
	v_pk_mul_f32 v[172:173], v[2:3], v[172:173] op_sel:[1,0]
	v_pk_fma_f32 v[144:145], v[144:145], v[174:175], v[176:177]
	v_cvt_pk_bf16_f32 v140, v140, v141
	v_pk_fma_f32 v[146:147], v[146:147], v[172:173], v[178:179]
	v_cvt_pk_bf16_f32 v141, v142, v143
	v_cvt_pk_bf16_f32 v144, v144, v145
	s_nop 0
	v_cvt_pk_bf16_f32 v145, v146, v147
	ds_write_b16 v60, v140 offset:44544
	ds_write_b16_d16_hi v60, v140 offset:44816
	ds_write_b16 v60, v141 offset:45088
	ds_write_b16_d16_hi v60, v141 offset:45360
	ds_write_b16 v60, v144 offset:45632
	ds_write_b16_d16_hi v60, v144 offset:45904
	ds_write_b16 v60, v145 offset:46176
	ds_write_b16_d16_hi v60, v145 offset:46448
	s_waitcnt vmcnt(14)
	v_lshlrev_b32_e32 v41, 16, v124
	v_and_b32_e32 v54, 0xffff0000, v124
	v_lshlrev_b32_e32 v52, 16, v125
	v_and_b32_e32 v53, 0xffff0000, v125
	v_lshlrev_b32_e32 v63, 16, v126
	v_and_b32_e32 v64, 0xffff0000, v126
	v_lshlrev_b32_e32 v65, 16, v127
	v_and_b32_e32 v66, 0xffff0000, v127
	v_sub_f32_e32 v53, v53, v2
	v_sub_f32_e32 v52, v52, v2
	v_sub_f32_e32 v55, v54, v2
	v_sub_f32_e32 v54, v41, v2
	v_pk_mul_f32 v[52:53], v[2:3], v[52:53] op_sel:[1,0]
	v_pk_mul_f32 v[54:55], v[2:3], v[54:55] op_sel:[1,0]
	v_pk_fma_f32 v[150:151], v[150:151], v[52:53], v[182:183]
	v_sub_f32_e32 v183, v64, v2
	v_sub_f32_e32 v182, v63, v2
	v_pk_fma_f32 v[148:149], v[148:149], v[54:55], v[180:181]
	v_sub_f32_e32 v181, v66, v2
	v_sub_f32_e32 v180, v65, v2
	v_pk_mul_f32 v[182:183], v[2:3], v[182:183] op_sel:[1,0]
	v_pk_mul_f32 v[180:181], v[2:3], v[180:181] op_sel:[1,0]
	v_pk_fma_f32 v[152:153], v[152:153], v[182:183], v[184:185]
	v_cvt_pk_bf16_f32 v148, v148, v149
	v_pk_fma_f32 v[154:155], v[154:155], v[180:181], v[186:187]
	v_cvt_pk_bf16_f32 v149, v150, v151
	v_cvt_pk_bf16_f32 v152, v152, v153
	s_nop 0
	v_cvt_pk_bf16_f32 v153, v154, v155
	ds_write_b16 v60, v148 offset:53248
	ds_write_b16_d16_hi v60, v148 offset:53520
	ds_write_b16 v60, v149 offset:53792
	ds_write_b16_d16_hi v60, v149 offset:54064
	ds_write_b16 v60, v152 offset:54336
	ds_write_b16_d16_hi v60, v152 offset:54608
	ds_write_b16 v60, v153 offset:54880
	ds_write_b16_d16_hi v60, v153 offset:55152
	s_waitcnt vmcnt(12)
; __device__ __forceinline__ void unpk8(const u32x4 w, f32x4& a, f32x4& b) { a = (f32x4){bflo(w.x), bfhi(w.x), bflo(w.y), bfhi(w.y)}; b = (f32x4){bflo(w.z), bfhi(w.z), bflo(w.w), bfhi(w.w)}; }
; __device__ __forceinline__ u32x4 pk8(const f32x4 a, const f32x4 b) { u32x4 w; w.x = cvt_pk_bf16(a[0], a[1]); w.y = cvt_pk_bf16(a[2], a[3]); w.z = cvt_pk_bf16(b[0], b[1]); w.w = cvt_pk_bf16(b[2], b[3]); return w; }
; #define LAS __attribute__((address_space(3)))
; __device__ __forceinline__ void gmlp_unit(Frame& F, const Args& a, int layer, int unit) {
;     ...
;         for (int i = 0; i < 4; ++i) { const int pc = tid + 512 * i, rr = pc >> 4, c16 = pc & 15;
;             *(LAS v4u*)(sA + rr * TP + c16 * 8) = *(const v4u*)(GMW + (size_t)g * 16384 + rr * 128 + c16 * 8); }
;         { const int p = tid & 127, oc0 = tid >> 7; const float mean = st[p * 2], rstd = st[p * 2 + 1];
; #pragma unroll
;           for (int i = 0; i < 4; ++i) { const int oc = oc0 + 4 * i, c0 = g * 128 + oc * 8;
;               f32x4 x0, x1; unpk8(*(const v4u*)(GUV + (t0 + p) * 2048 + 1024 + c0), x0, x1);
;               const f32x4 g0 = *(const f32x4*)(lng + c0), g1 = *(const f32x4*)(lng + c0 + 4), b0 = *(const f32x4*)(lnb + c0), b1 = *(const f32x4*)(lnb + c0 + 4);
;               x0 = (x0 - mean) * rstd * g0 + b0; x1 = (x1 - mean) * rstd * g1 + b1;
;               const v4u w = pk8(x0, x1);
;               LAS bf16* d = sB + (oc * 8) * TP + p;
;               d[0 * TP] = (bf16)(w.x & 0xffffu); d[1 * TP] = (bf16)(w.x >> 16); d[2 * TP] = (bf16)(w.y & 0xffffu); d[3 * TP] = (bf16)(w.y >> 16);
;               d[4 * TP] = (bf16)(w.z & 0xffffu); d[5 * TP] = (bf16)(w.z >> 16); d[6 * TP] = (bf16)(w.w & 0xffffu); d[7 * TP] = (bf16)(w.w >> 16); } }
;         __syncthreads();
;         f32x4 acc[4][2];
; #pragma unroll
;         for (int mt = 0; mt < 4; ++mt)
; #pragma unroll
;             for (int nt = 0; nt < 2; ++nt) acc[mt][nt] = (f32x4){0.f, 0.f, 0.f, 0.f};
;         mma_128(sA, sB, wave, lane, acc);
	v_lshlrev_b32_e32 v41, 16, v128
	v_and_b32_e32 v54, 0xffff0000, v128
	v_lshlrev_b32_e32 v52, 16, v129
	v_and_b32_e32 v53, 0xffff0000, v129
	v_lshlrev_b32_e32 v63, 16, v130
	v_and_b32_e32 v64, 0xffff0000, v130
	v_lshlrev_b32_e32 v65, 16, v131
	v_and_b32_e32 v66, 0xffff0000, v131
	v_sub_f32_e32 v53, v53, v2
	v_sub_f32_e32 v52, v52, v2
	v_sub_f32_e32 v55, v54, v2
	v_sub_f32_e32 v54, v41, v2
	v_pk_mul_f32 v[52:53], v[2:3], v[52:53] op_sel:[1,0]
	v_pk_mul_f32 v[54:55], v[2:3], v[54:55] op_sel:[1,0]
	v_pk_fma_f32 v[158:159], v[158:159], v[52:53], v[190:191]
	v_sub_f32_e32 v191, v64, v2
	v_sub_f32_e32 v190, v63, v2
	v_pk_fma_f32 v[156:157], v[156:157], v[54:55], v[188:189]
	v_sub_f32_e32 v189, v66, v2
	v_sub_f32_e32 v188, v65, v2
	v_pk_mul_f32 v[190:191], v[2:3], v[190:191] op_sel:[1,0]
	v_pk_mul_f32 v[188:189], v[2:3], v[188:189] op_sel:[1,0]
	v_pk_fma_f32 v[160:161], v[160:161], v[190:191], v[192:193]
	v_cvt_pk_bf16_f32 v156, v156, v157
	v_pk_fma_f32 v[162:163], v[162:163], v[188:189], v[194:195]
	v_cvt_pk_bf16_f32 v157, v158, v159
	v_cvt_pk_bf16_f32 v160, v160, v161
	s_nop 0
	v_cvt_pk_bf16_f32 v161, v162, v163
	ds_write_b16 v60, v156 offset:61952
	ds_write_b16_d16_hi v60, v156 offset:62224
	ds_write_b16 v60, v157 offset:62496
	ds_write_b16_d16_hi v60, v157 offset:62768
	ds_write_b16 v60, v160 offset:63040
	ds_write_b16_d16_hi v60, v160 offset:63312
	ds_write_b16 v60, v161 offset:63584
	ds_write_b16_d16_hi v60, v161 offset:63856
	s_waitcnt lgkmcnt(0)
	s_barrier
	s_add_u32 s22, s22, 0x200
	s_addc_u32 s23, s23, 0
	s_cmpk_eq_i32 s22, 0x1000
	s_cbranch_scc1 .Lgm_u2_last
	v_lshl_add_u64 v[72:73], s[6:7], 0, v[34:35]
	global_load_dwordx4 v[100:103], v[72:73], off
	v_lshl_add_u64 v[34:35], v[34:35], 0, s[34:35]
	v_lshl_add_u64 v[72:73], s[6:7], 0, v[36:37]
	global_load_dwordx4 v[104:107], v[72:73], off
	v_lshl_add_u64 v[36:37], v[36:37], 0, s[34:35]
	v_lshl_add_u64 v[72:73], s[6:7], 0, v[42:43]
	global_load_dwordx4 v[108:111], v[72:73], off
	v_lshl_add_u64 v[42:43], v[42:43], 0, s[34:35]
	v_lshl_add_u64 v[72:73], s[6:7], 0, v[46:47]
	global_load_dwordx4 v[112:115], v[72:73], off
	v_lshl_add_u64 v[46:47], v[46:47], 0, s[34:35]
	v_lshl_add_u64 v[74:75], s[6:7], 0, v[44:45]
	v_lshl_add_u64 v[70:71], v[48:49], 0, s[22:23]
	v_lshl_add_u64 v[44:45], v[44:45], 0, s[66:67]
	global_load_dwordx4 v[116:119], v[74:75], off offset:-128
	global_load_dwordx4 v[120:123], v[74:75], off offset:-64
	global_load_dwordx4 v[124:127], v[74:75], off
	global_load_dwordx4 v[128:131], v[74:75], off offset:64
	global_load_dwordx4 v[164:167], v[70:71], off
	global_load_dwordx4 v[168:171], v[70:71], off offset:16
	global_load_dwordx4 v[172:175], v[70:71], off offset:128
	global_load_dwordx4 v[176:179], v[70:71], off offset:144
	global_load_dwordx4 v[180:183], v[70:71], off offset:256
	global_load_dwordx4 v[184:187], v[70:71], off offset:272
	global_load_dwordx4 v[188:191], v[70:71], off offset:384
	global_load_dwordx4 v[192:195], v[70:71], off offset:400
	ds_read_b128 v[2:5], v61 offset:1024
	ds_read_b128 v[6:9], v61 offset:5376
	ds_read_b128 v[10:13], v61 offset:9728
	ds_read_b128 v[14:17], v61 offset:14080
	ds_read_b128 v[18:21], v62 offset:35840
	ds_read_b128 v[22:25], v62 offset:40192
	ds_read_b128 v[84:87], v61 offset:1088
	ds_read_b128 v[88:91], v61 offset:5440
	ds_read_b128 v[92:95], v61 offset:9792
	ds_read_b128 v[96:99], v61 offset:14144
	ds_read_b128 v[76:79], v62 offset:35904
	ds_read_b128 v[80:83], v62 offset:40256
	s_waitcnt lgkmcnt(6)
	v_mfma_f32_16x16x32_bf16 v[132:135], v[18:21], v[2:5], 0
	v_mfma_f32_16x16x32_bf16 v[136:139], v[22:25], v[2:5], 0
	v_mfma_f32_16x16x32_bf16 v[140:143], v[18:21], v[6:9], 0
	v_mfma_f32_16x16x32_bf16 v[144:147], v[22:25], v[6:9], 0
	v_mfma_f32_16x16x32_bf16 v[148:151], v[18:21], v[10:13], 0
	v_mfma_f32_16x16x32_bf16 v[152:155], v[22:25], v[10:13], 0
	v_mfma_f32_16x16x32_bf16 v[156:159], v[18:21], v[14:17], 0
	v_mfma_f32_16x16x32_bf16 v[160:163], v[22:25], v[14:17], 0
	ds_read_b128 v[2:5], v61 offset:1152
	ds_read_b128 v[6:9], v61 offset:5504
	ds_read_b128 v[10:13], v61 offset:9856
	ds_read_b128 v[14:17], v61 offset:14208
	ds_read_b128 v[18:21], v62 offset:35968
	ds_read_b128 v[22:25], v62 offset:40320
	s_waitcnt lgkmcnt(6)
	v_mfma_f32_16x16x32_bf16 v[132:135], v[76:79], v[84:87], v[132:135]
	v_mfma_f32_16x16x32_bf16 v[136:139], v[80:83], v[84:87], v[136:139]
	v_mfma_f32_16x16x32_bf16 v[140:143], v[76:79], v[88:91], v[140:143]
	v_mfma_f32_16x16x32_bf16 v[144:147], v[80:83], v[88:91], v[144:147]
	v_mfma_f32_16x16x32_bf16 v[148:151], v[76:79], v[92:95], v[148:151]
	v_mfma_f32_16x16x32_bf16 v[152:155], v[80:83], v[92:95], v[152:155]
	v_mfma_f32_16x16x32_bf16 v[156:159], v[76:79], v[96:99], v[156:159]
	v_mfma_f32_16x16x32_bf16 v[160:163], v[80:83], v[96:99], v[160:163]
	ds_read_b128 v[84:87], v61 offset:1216
	ds_read_b128 v[88:91], v61 offset:5568
	ds_read_b128 v[92:95], v61 offset:9920
	ds_read_b128 v[96:99], v61 offset:14272
	ds_read_b128 v[76:79], v62 offset:36032
	ds_read_b128 v[80:83], v62 offset:40384
	s_waitcnt lgkmcnt(6)
	v_mfma_f32_16x16x32_bf16 v[132:135], v[18:21], v[2:5], v[132:135]
	v_mfma_f32_16x16x32_bf16 v[136:139], v[22:25], v[2:5], v[136:139]
	v_mfma_f32_16x16x32_bf16 v[140:143], v[18:21], v[6:9], v[140:143]
	v_mfma_f32_16x16x32_bf16 v[144:147], v[22:25], v[6:9], v[144:147]
	v_mfma_f32_16x16x32_bf16 v[148:151], v[18:21], v[10:13], v[148:151]
	v_mfma_f32_16x16x32_bf16 v[152:155], v[22:25], v[10:13], v[152:155]
	v_mfma_f32_16x16x32_bf16 v[156:159], v[18:21], v[14:17], v[156:159]
	v_mfma_f32_16x16x32_bf16 v[160:163], v[22:25], v[14:17], v[160:163]
	s_waitcnt lgkmcnt(0)
; __device__ __forceinline__ unsigned cvt_pk_bf16(float lo, float hi) { unsigned r; asm volatile("v_cvt_pk_bf16_f32 %0, %1, %2" : "=v"(r) : "v"(lo), "v"(hi)); return r; }
; __device__ __forceinline__ void gmlp_unit(Frame& F, const Args& a, int layer, int unit) {
;     ...
;         mma_128(sA, sB, wave, lane, acc);
;         { const int wm = wave >> 2, wn = wave & 3, fr = lane & 15, fq = lane >> 4;
; #pragma unroll
;           for (int mt = 0; mt < 4; ++mt) { const int tt = 64 * wm + 16 * mt + fr; const float bsv = bsp[g * 128 + tt];
; #pragma unroll
;               for (int nt = 0; nt < 2; ++nt) { const int c = g * 128 + 32 * wn + 16 * nt + 4 * fq;
;                   const v2u uw = *(const v2u*)(GUV + (t0 + tt) * 2048 + c);
;                   const f32x4 u4 = (f32x4){bflo(uw.x), bfhi(uw.x), bflo(uw.y), bfhi(uw.y)};
;                   const f32x4 yb = u4 * (acc[mt][nt] + bsv);
;                   v2u ow; ow.x = cvt_pk_bf16(yb.x, yb.y); ow.y = cvt_pk_bf16(yb.z, yb.w);
;                   *(v2u*)(GUV + (t0 + tt) * 2048 + c) = ow; } } }
;         __syncthreads();
	v_mfma_f32_16x16x32_bf16 v[132:135], v[76:79], v[84:87], v[132:135]
	v_mfma_f32_16x16x32_bf16 v[136:139], v[80:83], v[84:87], v[136:139]
	v_mfma_f32_16x16x32_bf16 v[140:143], v[76:79], v[88:91], v[140:143]
	v_mfma_f32_16x16x32_bf16 v[144:147], v[80:83], v[88:91], v[144:147]
	v_mfma_f32_16x16x32_bf16 v[148:151], v[76:79], v[92:95], v[148:151]
	v_mfma_f32_16x16x32_bf16 v[152:155], v[80:83], v[92:95], v[152:155]
	v_mfma_f32_16x16x32_bf16 v[156:159], v[76:79], v[96:99], v[156:159]
	v_mfma_f32_16x16x32_bf16 v[160:163], v[80:83], v[96:99], v[160:163]
	s_nop 7
	s_nop 1
	s_waitcnt vmcnt(25)
	v_lshlrev_b32_e32 v70, 16, v204
	v_and_b32_e32 v71, 0xffff0000, v204
	v_lshlrev_b32_e32 v68, 16, v205
	v_and_b32_e32 v69, 0xffff0000, v205
	v_pk_add_f32 v[72:73], v[134:135], v[196:197] op_sel_hi:[1,0]
	v_pk_add_f32 v[74:75], v[132:133], v[196:197] op_sel_hi:[1,0]
	v_pk_mul_f32 v[68:69], v[72:73], v[68:69]
	v_pk_mul_f32 v[70:71], v[74:75], v[70:71]
	v_cvt_pk_bf16_f32 v70, v70, v71
	v_cvt_pk_bf16_f32 v71, v68, v69
	global_store_dwordx2 v[232:233], v[70:71], off
	v_lshlrev_b32_e32 v16, 16, v206
	v_and_b32_e32 v17, 0xffff0000, v206
	v_lshlrev_b32_e32 v18, 16, v207
	v_and_b32_e32 v19, 0xffff0000, v207
	v_pk_add_f32 v[20:21], v[136:137], v[196:197] op_sel_hi:[1,0]
	v_pk_add_f32 v[22:23], v[138:139], v[196:197] op_sel_hi:[1,0]
	v_pk_mul_f32 v[20:21], v[20:21], v[16:17]
	v_pk_mul_f32 v[22:23], v[22:23], v[18:19]
	v_cvt_pk_bf16_f32 v20, v20, v21
	s_nop 0
	v_cvt_pk_bf16_f32 v21, v22, v23
	global_store_dwordx2 v[232:233], v[20:21], off offset:32
	s_waitcnt vmcnt(24)
	v_lshlrev_b32_e32 v70, 16, v224
	v_and_b32_e32 v71, 0xffff0000, v224
	v_lshlrev_b32_e32 v68, 16, v225
	v_and_b32_e32 v69, 0xffff0000, v225
	v_pk_add_f32 v[72:73], v[142:143], v[198:199] op_sel_hi:[1,0]
	v_pk_add_f32 v[74:75], v[140:141], v[198:199] op_sel_hi:[1,0]
	v_pk_mul_f32 v[68:69], v[72:73], v[68:69]
	v_pk_mul_f32 v[70:71], v[74:75], v[70:71]
	v_cvt_pk_bf16_f32 v70, v70, v71
	v_cvt_pk_bf16_f32 v71, v68, v69
	global_store_dwordx2 v[234:235], v[70:71], off
	v_lshlrev_b32_e32 v16, 16, v226
	v_and_b32_e32 v17, 0xffff0000, v226
	v_lshlrev_b32_e32 v18, 16, v227
	v_and_b32_e32 v19, 0xffff0000, v227
	v_pk_add_f32 v[20:21], v[144:145], v[198:199] op_sel_hi:[1,0]
	v_pk_add_f32 v[22:23], v[146:147], v[198:199] op_sel_hi:[1,0]
	v_pk_mul_f32 v[20:21], v[20:21], v[16:17]
	v_pk_mul_f32 v[22:23], v[22:23], v[18:19]
	v_cvt_pk_bf16_f32 v20, v20, v21
	s_nop 0
	v_cvt_pk_bf16_f32 v21, v22, v23
	global_store_dwordx2 v[234:235], v[20:21], off offset:32
	s_waitcnt vmcnt(23)
	v_lshlrev_b32_e32 v70, 16, v228
	v_and_b32_e32 v71, 0xffff0000, v228
	v_lshlrev_b32_e32 v68, 16, v229
	v_and_b32_e32 v69, 0xffff0000, v229
	v_pk_add_f32 v[72:73], v[150:151], v[200:201] op_sel_hi:[1,0]
	v_pk_add_f32 v[74:75], v[148:149], v[200:201] op_sel_hi:[1,0]
	v_pk_mul_f32 v[68:69], v[72:73], v[68:69]
	v_pk_mul_f32 v[70:71], v[74:75], v[70:71]
	v_cvt_pk_bf16_f32 v70, v70, v71
	v_cvt_pk_bf16_f32 v71, v68, v69
	global_store_dwordx2 v[236:237], v[70:71], off
	v_lshlrev_b32_e32 v16, 16, v230
	v_and_b32_e32 v17, 0xffff0000, v230
	v_lshlrev_b32_e32 v18, 16, v231
	v_and_b32_e32 v19, 0xffff0000, v231
	v_pk_add_f32 v[20:21], v[152:153], v[200:201] op_sel_hi:[1,0]
	v_pk_add_f32 v[22:23], v[154:155], v[200:201] op_sel_hi:[1,0]
	v_pk_mul_f32 v[20:21], v[20:21], v[16:17]
	v_pk_mul_f32 v[22:23], v[22:23], v[18:19]
	v_cvt_pk_bf16_f32 v20, v20, v21
	s_nop 0
	v_cvt_pk_bf16_f32 v21, v22, v23
	global_store_dwordx2 v[236:237], v[20:21], off offset:32
	s_waitcnt vmcnt(22)
	v_lshlrev_b32_e32 v70, 16, v246
	v_and_b32_e32 v71, 0xffff0000, v246
	v_lshlrev_b32_e32 v68, 16, v247
	v_and_b32_e32 v69, 0xffff0000, v247
	v_pk_add_f32 v[72:73], v[158:159], v[202:203] op_sel_hi:[1,0]
	v_pk_add_f32 v[74:75], v[156:157], v[202:203] op_sel_hi:[1,0]
	v_pk_mul_f32 v[68:69], v[72:73], v[68:69]
	v_pk_mul_f32 v[70:71], v[74:75], v[70:71]
	v_cvt_pk_bf16_f32 v70, v70, v71
	v_cvt_pk_bf16_f32 v71, v68, v69
	global_store_dwordx2 v[238:239], v[70:71], off
	v_lshlrev_b32_e32 v16, 16, v248
	v_and_b32_e32 v17, 0xffff0000, v248
	v_lshlrev_b32_e32 v18, 16, v249
	v_and_b32_e32 v19, 0xffff0000, v249
	v_pk_add_f32 v[20:21], v[160:161], v[202:203] op_sel_hi:[1,0]
	v_pk_add_f32 v[22:23], v[162:163], v[202:203] op_sel_hi:[1,0]
	v_pk_mul_f32 v[20:21], v[20:21], v[16:17]
	v_pk_mul_f32 v[22:23], v[22:23], v[18:19]
	v_cvt_pk_bf16_f32 v20, v20, v21
	s_nop 0
	v_cvt_pk_bf16_f32 v21, v22, v23
	global_store_dwordx2 v[238:239], v[20:21], off offset:32
	s_barrier
	s_branch .LBB0_839
; #define LAS __attribute__((address_space(3)))
; __device__ __forceinline__ void mma_128(const LAS bf16* sA, const LAS bf16* sBt, int wave, int lane, f32x4 (&acc)[4][2]) {
;     const int wm = wave >> 2, wn = wave & 3, fr = lane & 15, fq = lane >> 4;
; #pragma unroll
;     for (int kk = 0; kk < 4; ++kk) {
;         bf16x8 af[4], bf_[2];
; #pragma unroll
;         for (int mt = 0; mt < 4; ++mt) af[mt] = *(const LAS bf16x8*)(sA + (64 * wm + 16 * mt + fr) * TP + 32 * kk + 8 * fq);
; #pragma unroll
;         for (int nt = 0; nt < 2; ++nt) bf_[nt] = *(const LAS bf16x8*)(sBt + (32 * wn + 16 * nt + fr) * TP + 32 * kk + 8 * fq);
; #pragma unroll
;         for (int mt = 0; mt < 4; ++mt)
; #pragma unroll
;             for (int nt = 0; nt < 2; ++nt) acc[mt][nt] = __builtin_amdgcn_mfma_f32_16x16x32_bf16(bf_[nt], af[mt], acc[mt][nt], 0, 0, 0);
;     }
; }
.Lgm_u2_last:
	ds_read_b128 v[2:5], v61 offset:1024
	ds_read_b128 v[6:9], v61 offset:5376
	ds_read_b128 v[10:13], v61 offset:9728
	ds_read_b128 v[14:17], v61 offset:14080
	ds_read_b128 v[18:21], v62 offset:35840
	ds_read_b128 v[22:25], v62 offset:40192
	ds_read_b128 v[84:87], v61 offset:1088
	ds_read_b128 v[88:91], v61 offset:5440
	ds_read_b128 v[92:95], v61 offset:9792
	ds_read_b128 v[96:99], v61 offset:14144
	ds_read_b128 v[76:79], v62 offset:35904
	ds_read_b128 v[80:83], v62 offset:40256
	s_waitcnt lgkmcnt(6)
	v_mfma_f32_16x16x32_bf16 v[132:135], v[18:21], v[2:5], 0
	v_mfma_f32_16x16x32_bf16 v[136:139], v[22:25], v[2:5], 0
	v_mfma_f32_16x16x32_bf16 v[140:143], v[18:21], v[6:9], 0
	v_mfma_f32_16x16x32_bf16 v[144:147], v[22:25], v[6:9], 0
	v_mfma_f32_16x16x32_bf16 v[148:151], v[18:21], v[10:13], 0
	v_mfma_f32_16x16x32_bf16 v[152:155], v[22:25], v[10:13], 0
	v_mfma_f32_16x16x32_bf16 v[156:159], v[18:21], v[14:17], 0
	v_mfma_f32_16x16x32_bf16 v[160:163], v[22:25], v[14:17], 0
	ds_read_b128 v[2:5], v61 offset:1152
	ds_read_b128 v[6:9], v61 offset:5504
	ds_read_b128 v[10:13], v61 offset:9856
	ds_read_b128 v[14:17], v61 offset:14208
	ds_read_b128 v[18:21], v62 offset:35968
	ds_read_b128 v[22:25], v62 offset:40320
	s_waitcnt lgkmcnt(6)
	v_mfma_f32_16x16x32_bf16 v[132:135], v[76:79], v[84:87], v[132:135]
	v_mfma_f32_16x16x32_bf16 v[136:139], v[80:83], v[84:87], v[136:139]
	v_mfma_f32_16x16x32_bf16 v[140:143], v[76:79], v[88:91], v[140:143]
	v_mfma_f32_16x16x32_bf16 v[144:147], v[80:83], v[88:91], v[144:147]
	v_mfma_f32_16x16x32_bf16 v[148:151], v[76:79], v[92:95], v[148:151]
	v_mfma_f32_16x16x32_bf16 v[152:155], v[80:83], v[92:95], v[152:155]
	v_mfma_f32_16x16x32_bf16 v[156:159], v[76:79], v[96:99], v[156:159]
	v_mfma_f32_16x16x32_bf16 v[160:163], v[80:83], v[96:99], v[160:163]
	ds_read_b128 v[84:87], v61 offset:1216
	ds_read_b128 v[88:91], v61 offset:5568
	ds_read_b128 v[92:95], v61 offset:9920
	ds_read_b128 v[96:99], v61 offset:14272
	ds_read_b128 v[76:79], v62 offset:36032
	ds_read_b128 v[80:83], v62 offset:40384
	s_waitcnt lgkmcnt(6)
	v_mfma_f32_16x16x32_bf16 v[132:135], v[18:21], v[2:5], v[132:135]
	v_mfma_f32_16x16x32_bf16 v[136:139], v[22:25], v[2:5], v[136:139]
	v_mfma_f32_16x16x32_bf16 v[140:143], v[18:21], v[6:9], v[140:143]
	v_mfma_f32_16x16x32_bf16 v[144:147], v[22:25], v[6:9], v[144:147]
	v_mfma_f32_16x16x32_bf16 v[148:151], v[18:21], v[10:13], v[148:151]
	v_mfma_f32_16x16x32_bf16 v[152:155], v[22:25], v[10:13], v[152:155]
	v_mfma_f32_16x16x32_bf16 v[156:159], v[18:21], v[14:17], v[156:159]
	v_mfma_f32_16x16x32_bf16 v[160:163], v[22:25], v[14:17], v[160:163]
	s_waitcnt lgkmcnt(0)
	v_mfma_f32_16x16x32_bf16 v[132:135], v[76:79], v[84:87], v[132:135]
	v_mfma_f32_16x16x32_bf16 v[136:139], v[80:83], v[84:87], v[136:139]
	v_mfma_f32_16x16x32_bf16 v[140:143], v[76:79], v[88:91], v[140:143]
	v_mfma_f32_16x16x32_bf16 v[144:147], v[80:83], v[88:91], v[144:147]
	v_mfma_f32_16x16x32_bf16 v[148:151], v[76:79], v[92:95], v[148:151]
	v_mfma_f32_16x16x32_bf16 v[152:155], v[80:83], v[92:95], v[152:155]
	v_mfma_f32_16x16x32_bf16 v[156:159], v[76:79], v[96:99], v[156:159]
	v_mfma_f32_16x16x32_bf16 v[160:163], v[80:83], v[96:99], v[160:163]
	s_nop 7
	s_nop 1
	s_waitcnt vmcnt(9)
; __device__ __forceinline__ unsigned cvt_pk_bf16(float lo, float hi) { unsigned r; asm volatile("v_cvt_pk_bf16_f32 %0, %1, %2" : "=v"(r) : "v"(lo), "v"(hi)); return r; }
; __device__ __forceinline__ void gmlp_unit(Frame& F, const Args& a, int layer, int unit) {
;     ...
;         { const int wm = wave >> 2, wn = wave & 3, fr = lane & 15, fq = lane >> 4;
; #pragma unroll
;           for (int mt = 0; mt < 4; ++mt) { const int tt = 64 * wm + 16 * mt + fr; const float bsv = bsp[g * 128 + tt];
; #pragma unroll
;               for (int nt = 0; nt < 2; ++nt) { const int c = g * 128 + 32 * wn + 16 * nt + 4 * fq;
;                   const v2u uw = *(const v2u*)(GUV + (t0 + tt) * 2048 + c);
;                   const f32x4 u4 = (f32x4){bflo(uw.x), bfhi(uw.x), bflo(uw.y), bfhi(uw.y)};
;                   const f32x4 yb = u4 * (acc[mt][nt] + bsv);
;                   v2u ow; ow.x = cvt_pk_bf16(yb.x, yb.y); ow.y = cvt_pk_bf16(yb.z, yb.w);
;                   *(v2u*)(GUV + (t0 + tt) * 2048 + c) = ow; } } }
;         __syncthreads();
;     }
	v_lshlrev_b32_e32 v70, 16, v204
	v_and_b32_e32 v71, 0xffff0000, v204
	v_lshlrev_b32_e32 v68, 16, v205
	v_and_b32_e32 v69, 0xffff0000, v205
	v_pk_add_f32 v[72:73], v[134:135], v[196:197] op_sel_hi:[1,0]
	v_pk_add_f32 v[74:75], v[132:133], v[196:197] op_sel_hi:[1,0]
	v_pk_mul_f32 v[68:69], v[72:73], v[68:69]
	v_pk_mul_f32 v[70:71], v[74:75], v[70:71]
	v_cvt_pk_bf16_f32 v70, v70, v71
	v_cvt_pk_bf16_f32 v71, v68, v69
	global_store_dwordx2 v[232:233], v[70:71], off
	v_lshlrev_b32_e32 v16, 16, v206
	v_and_b32_e32 v17, 0xffff0000, v206
	v_lshlrev_b32_e32 v18, 16, v207
	v_and_b32_e32 v19, 0xffff0000, v207
	v_pk_add_f32 v[20:21], v[136:137], v[196:197] op_sel_hi:[1,0]
	v_pk_add_f32 v[22:23], v[138:139], v[196:197] op_sel_hi:[1,0]
	v_pk_mul_f32 v[20:21], v[20:21], v[16:17]
	v_pk_mul_f32 v[22:23], v[22:23], v[18:19]
	v_cvt_pk_bf16_f32 v20, v20, v21
	s_nop 0
	v_cvt_pk_bf16_f32 v21, v22, v23
	global_store_dwordx2 v[232:233], v[20:21], off offset:32
	s_waitcnt vmcnt(8)
	v_lshlrev_b32_e32 v70, 16, v224
	v_and_b32_e32 v71, 0xffff0000, v224
	v_lshlrev_b32_e32 v68, 16, v225
	v_and_b32_e32 v69, 0xffff0000, v225
	v_pk_add_f32 v[72:73], v[142:143], v[198:199] op_sel_hi:[1,0]
	v_pk_add_f32 v[74:75], v[140:141], v[198:199] op_sel_hi:[1,0]
	v_pk_mul_f32 v[68:69], v[72:73], v[68:69]
	v_pk_mul_f32 v[70:71], v[74:75], v[70:71]
	v_cvt_pk_bf16_f32 v70, v70, v71
	v_cvt_pk_bf16_f32 v71, v68, v69
	global_store_dwordx2 v[234:235], v[70:71], off
	v_lshlrev_b32_e32 v16, 16, v226
	v_and_b32_e32 v17, 0xffff0000, v226
	v_lshlrev_b32_e32 v18, 16, v227
	v_and_b32_e32 v19, 0xffff0000, v227
	v_pk_add_f32 v[20:21], v[144:145], v[198:199] op_sel_hi:[1,0]
	v_pk_add_f32 v[22:23], v[146:147], v[198:199] op_sel_hi:[1,0]
	v_pk_mul_f32 v[20:21], v[20:21], v[16:17]
	v_pk_mul_f32 v[22:23], v[22:23], v[18:19]
	v_cvt_pk_bf16_f32 v20, v20, v21
	s_nop 0
	v_cvt_pk_bf16_f32 v21, v22, v23
	global_store_dwordx2 v[234:235], v[20:21], off offset:32
	s_waitcnt vmcnt(7)
	v_lshlrev_b32_e32 v70, 16, v228
	v_and_b32_e32 v71, 0xffff0000, v228
	v_lshlrev_b32_e32 v68, 16, v229
	v_and_b32_e32 v69, 0xffff0000, v229
	v_pk_add_f32 v[72:73], v[150:151], v[200:201] op_sel_hi:[1,0]
	v_pk_add_f32 v[74:75], v[148:149], v[200:201] op_sel_hi:[1,0]
	v_pk_mul_f32 v[68:69], v[72:73], v[68:69]
	v_pk_mul_f32 v[70:71], v[74:75], v[70:71]
	v_cvt_pk_bf16_f32 v70, v70, v71
	v_cvt_pk_bf16_f32 v71, v68, v69
	global_store_dwordx2 v[236:237], v[70:71], off
	v_lshlrev_b32_e32 v16, 16, v230
	v_and_b32_e32 v17, 0xffff0000, v230
	v_lshlrev_b32_e32 v18, 16, v231
	v_and_b32_e32 v19, 0xffff0000, v231
	v_pk_add_f32 v[20:21], v[152:153], v[200:201] op_sel_hi:[1,0]
	v_pk_add_f32 v[22:23], v[154:155], v[200:201] op_sel_hi:[1,0]
	v_pk_mul_f32 v[20:21], v[20:21], v[16:17]
	v_pk_mul_f32 v[22:23], v[22:23], v[18:19]
	v_cvt_pk_bf16_f32 v20, v20, v21
	s_nop 0
	v_cvt_pk_bf16_f32 v21, v22, v23
	global_store_dwordx2 v[236:237], v[20:21], off offset:32
	s_waitcnt vmcnt(6)
	v_lshlrev_b32_e32 v70, 16, v246
	v_and_b32_e32 v71, 0xffff0000, v246
	v_lshlrev_b32_e32 v68, 16, v247
	v_and_b32_e32 v69, 0xffff0000, v247
	v_pk_add_f32 v[72:73], v[158:159], v[202:203] op_sel_hi:[1,0]
	v_pk_add_f32 v[74:75], v[156:157], v[202:203] op_sel_hi:[1,0]
	v_pk_mul_f32 v[68:69], v[72:73], v[68:69]
	v_pk_mul_f32 v[70:71], v[74:75], v[70:71]
	v_cvt_pk_bf16_f32 v70, v70, v71
	v_cvt_pk_bf16_f32 v71, v68, v69
	global_store_dwordx2 v[238:239], v[70:71], off
	v_lshlrev_b32_e32 v16, 16, v248
	v_and_b32_e32 v17, 0xffff0000, v248
	v_lshlrev_b32_e32 v18, 16, v249
	v_and_b32_e32 v19, 0xffff0000, v249
	v_pk_add_f32 v[20:21], v[160:161], v[202:203] op_sel_hi:[1,0]
	v_pk_add_f32 v[22:23], v[162:163], v[202:203] op_sel_hi:[1,0]
	v_pk_mul_f32 v[20:21], v[20:21], v[16:17]
	v_pk_mul_f32 v[22:23], v[22:23], v[18:19]
	v_cvt_pk_bf16_f32 v20, v20, v21
	s_nop 0
	v_cvt_pk_bf16_f32 v21, v22, v23
	global_store_dwordx2 v[238:239], v[20:21], off offset:32
	s_barrier
	v_readlane_b32 s3, v254, 8
	s_add_i32 s5, s5, s3
	v_readlane_b32 s3, v254, 21
	s_add_i32 s20, s20, s3
	s_add_i32 s2, s2, s3
	s_cmpk_gt_i32 s5, 0x7f
	s_cbranch_scc0 .LBB0_828
